# speedup vs baseline: 1.0069x; 1.0069x over previous
_Z11prep_kernelPKfS0_S0_S0_PDF16_S1_S0_S1_:
	s_getpc_b64 s[24:25]
	v_lshlrev_b32_e32 v172, 7, v0
	v_min_u32_e32 v172, 0x5a00, v172
	global_load_dword v173, v172, s[24:25]
	s_load_dwordx8 s[4:11], s[0:1], 0x0
	s_load_dwordx4 s[12:15], s[0:1], 0x20
	s_mov_b32 s3, 0
	s_lshl_b64 s[2:3], s[2:3], 6
	v_cmp_gt_u32_e32 vcc, 8, v0
	v_lshlrev_b32_e32 v1, 3, v0
	s_and_saveexec_b64 s[16:17], vcc
	s_cbranch_execz .LBB0_2
	s_load_dwordx4 s[20:23], s[0:1], 0x30
	v_or_b32_e32 v10, s2, v1
	v_mov_b32_e32 v11, s3
	s_waitcnt lgkmcnt(0)
	v_lshl_add_u64 v[12:13], v[10:11], 2, s[20:21]
	global_load_dwordx4 v[2:5], v[12:13], off
	global_load_dwordx4 v[6:9], v[12:13], off offset:16
	s_waitcnt vmcnt(1)
	v_cvt_pk_f16_f32 v2, v2, v3
	v_cvt_pk_f16_f32 v3, v4, v5
	s_waitcnt vmcnt(0)
	v_cvt_pk_f16_f32 v4, v6, v7
	v_lshl_add_u64 v[6:7], v[10:11], 1, s[22:23]
	v_cvt_pk_f16_f32 v5, v8, v9
	global_store_dwordx4 v[6:7], v[2:5], off

	.amdhsa_kernel _Z11prep_kernelPKfS0_S0_S0_PDF16_S1_S0_S1_
		.amdhsa_group_segment_fixed_size 34816
		.amdhsa_private_segment_fixed_size 0
		.amdhsa_kernarg_size 64
		.amdhsa_user_sgpr_count 2
		.amdhsa_user_sgpr_dispatch_ptr 0
		.amdhsa_user_sgpr_queue_ptr 0
		.amdhsa_user_sgpr_kernarg_segment_ptr 1
		.amdhsa_user_sgpr_dispatch_id 0
		.amdhsa_user_sgpr_kernarg_preload_length 0
		.amdhsa_user_sgpr_kernarg_preload_offset 0
		.amdhsa_user_sgpr_private_segment_size 0
		.amdhsa_uses_dynamic_stack 0
		.amdhsa_enable_private_segment 0
		.amdhsa_system_sgpr_workgroup_id_x 1
		.amdhsa_system_sgpr_workgroup_id_y 0
		.amdhsa_system_sgpr_workgroup_id_z 0
		.amdhsa_system_sgpr_workgroup_info 0
		.amdhsa_system_vgpr_workitem_id 0
		.amdhsa_next_free_vgpr 208
		.amdhsa_next_free_sgpr 96
		.amdhsa_accum_offset 176
		.amdhsa_reserve_vcc 1
		.amdhsa_float_round_mode_32 0
		.amdhsa_float_round_mode_16_64 0
		.amdhsa_float_denorm_mode_32 3
		.amdhsa_float_denorm_mode_16_64 3
		.amdhsa_dx10_clamp 1
		.amdhsa_ieee_mode 1
		.amdhsa_fp16_overflow 0
		.amdhsa_tg_split 0
		.amdhsa_exception_fp_ieee_invalid_op 0
		.amdhsa_exception_fp_denorm_src 0
		.amdhsa_exception_fp_ieee_div_zero 0
		.amdhsa_exception_fp_ieee_overflow 0
		.amdhsa_exception_fp_ieee_underflow 0
		.amdhsa_exception_fp_ieee_inexact 0
		.amdhsa_exception_int_div_zero 0
	.end_amdhsa_kernel

_Z11attn_kernelPKDF16_S0_PDF16_P15HIP_vector_typeIfLj2EE:
	s_getpc_b64 s[38:39]
	v_lshlrev_b32_e32 v240, 7, v0
	v_min_u32_e32 v240, 0x3500, v240
	global_load_dword v241, v240, s[38:39]
	s_mov_b32 s5, 0
	s_mov_b32 s28, s3
	s_load_dwordx8 s[20:27], s[0:1], 0x0
	s_mov_b32 s3, s5
	s_lshl_b64 s[0:1], s[4:5], 12
	s_lshl_b64 s[2:3], s[2:3], 8
	s_add_u32 s0, s0, s2
	v_lshrrev_b32_e32 v1, 6, v0
	s_addc_u32 s1, s1, s3
	v_and_b32_e32 v160, 31, v0
	s_lshl_b64 s[2:3], s[0:1], 8
	v_lshlrev_b32_e32 v162, 5, v1
	s_waitcnt lgkmcnt(0)
	s_add_u32 s2, s20, s2
	v_or_b32_e32 v2, v162, v160
	v_bfe_u32 v54, v0, 5, 1
	s_addc_u32 s3, s21, s3
	v_lshlrev_b32_e32 v164, 8, v2
	v_mov_b32_e32 v165, 0
	v_lshl_add_u64 v[2:3], s[2:3], 0, v[164:165]
	v_lshlrev_b32_e32 v164, 4, v54
	v_lshl_add_u64 v[2:3], v[2:3], 0, v[164:165]
	global_load_dwordx4 v[156:159], v[2:3], off
	global_load_dwordx4 v[152:155], v[2:3], off offset:32
	global_load_dwordx4 v[148:151], v[2:3], off offset:64
	global_load_dwordx4 v[144:147], v[2:3], off offset:96
	global_load_dwordx4 v[140:143], v[2:3], off offset:128
	global_load_dwordx4 v[136:139], v[2:3], off offset:160
	global_load_dwordx4 v[132:135], v[2:3], off offset:192
	global_load_dwordx4 v[128:131], v[2:3], off offset:224
	s_ashr_i32 s29, s28, 31
	v_bfe_u32 v55, v0, 2, 3
	s_lshl_b64 s[2:3], s[4:5], 20
	s_lshl_b64 s[20:21], s[28:29], 18
	v_lshl_or_b32 v2, v1, 3, v55
	s_add_u32 s4, s22, s2
	v_lshrrev_b32_e32 v3, 2, v2
	s_addc_u32 s7, s23, s3
	v_xor_b32_e32 v4, v3, v0
	s_add_u32 s6, s4, s20
	v_and_b32_e32 v5, 32, v0
	v_lshlrev_b32_e32 v4, 3, v4
	v_lshlrev_b32_e32 v1, 11, v1
	s_addc_u32 s7, s7, s21
	v_lshlrev_b32_e32 v164, 8, v2
	v_and_or_b32 v4, v4, 24, v5
	v_add_u32_e32 v173, 0, v1
	v_lshl_add_u64 v[2:3], s[6:7], 0, v[164:165]
	v_lshlrev_b32_e32 v164, 1, v4
	v_readfirstlane_b32 s4, v173
	v_add_u32_e32 v6, 0x400, v173
	v_lshl_add_u64 v[2:3], v[2:3], 0, v[164:165]
	s_mov_b64 s[6:7], 0x80
	s_mov_b32 m0, s4
	v_readfirstlane_b32 s4, v6
	v_add_u32_e32 v6, 0x4000, v173
	v_lshl_add_u64 v[4:5], v[2:3], 0, s[6:7]
	global_load_lds_dwordx4 v[2:3], off
	s_mov_b32 m0, s4
	s_mov_b64 s[6:7], 0x4000
	v_readfirstlane_b32 s4, v6
	global_load_lds_dwordx4 v[4:5], off
	v_lshl_add_u64 v[4:5], v[2:3], 0, s[6:7]
	s_mov_b32 m0, s4
	s_mov_b64 s[6:7], 0x4080
	global_load_lds_dwordx4 v[4:5], off
	v_add_u32_e32 v4, 0x4400, v173
	v_lshl_add_u64 v[2:3], v[2:3], 0, s[6:7]
	v_readfirstlane_b32 s4, v4
	s_mov_b32 m0, s4
	s_movk_i32 s4, 0x1c0
	global_load_lds_dwordx4 v[2:3], off
	v_lshlrev_b32_e32 v2, 8, v0
	v_and_b32_e32 v2, 0x1800, v2
	v_lshlrev_b32_e32 v3, 6, v0
	v_and_or_b32 v6, v3, s4, v2
	v_xor_b32_e32 v2, v54, v55
	v_lshlrev_b32_e32 v2, 4, v2
	v_and_or_b32 v175, v2, 48, v6
	s_waitcnt vmcnt(2)
	v_add_u32_e32 v172, 0, v175
	s_waitcnt lgkmcnt(0)
	s_barrier
	ds_read_b128 v[2:5], v172
	ds_read_b128 v[34:37], v172 offset:512
	v_bitop3_b32 v7, v54, v55, 2 bitop3:0x36
	v_lshlrev_b32_e32 v7, 4, v7
	v_and_or_b32 v176, v7, 48, v6
	v_add_u32_e32 v174, 0, v176
	ds_read_b128 v[18:21], v174
	ds_read_b128 v[38:41], v174 offset:512
	s_mov_b32 s33, 0x41200000
	s_cmp_lg_u32 0, -1
	s_cselect_b32 s37, 0, 0
	s_waitcnt vmcnt(0) lgkmcnt(0)
	v_mfma_f32_32x32x16_f16 v[2:17], v[2:5], v[156:159], 0
	s_movk_i32 s4, 0x110
	v_and_b32_e32 v161, 63, v0
	v_lshl_or_b32 v1, v55, 8, v1
	s_mov_b32 s18, s5
	s_mov_b32 s19, s5
	s_mov_b32 s6, s5
	s_mov_b32 s7, s5
	v_mfma_f32_32x32x16_f16 v[2:17], v[18:21], v[152:155], v[2:17]
	ds_read_b128 v[18:21], v172 offset:8192
	ds_read_b128 v[42:45], v172 offset:8704
	ds_read_b128 v[46:49], v174 offset:8192
	ds_read_b128 v[50:53], v174 offset:8704
	s_mov_b32 s8, s5
	s_mov_b32 s9, s5
	s_mov_b32 s10, s5
	s_mov_b32 s11, s5
	s_mov_b32 s12, s5
	s_waitcnt lgkmcnt(3)
	v_mfma_f32_32x32x16_f16 v[18:33], v[18:21], v[156:159], 0
	s_mov_b32 s13, s5
	s_mov_b32 s14, s5
	s_mov_b32 s15, s5
	s_mov_b32 s16, s5
	s_mov_b32 s17, s5
	s_mov_b32 s36, 1
	s_mov_b32 s34, -1
	s_waitcnt lgkmcnt(1)
	v_mfma_f32_32x32x16_f16 v[18:33], v[46:49], v[152:155], v[18:33]
	s_mov_b32 s35, 2
	s_mov_b64 s[30:31], 0x8000
	v_mfma_f32_32x32x16_f16 v[2:17], v[34:37], v[148:151], v[2:17]
	v_mfma_f32_32x32x16_f16 v[18:33], v[42:45], v[148:151], v[18:33]
	v_mfma_f32_32x32x16_f16 v[2:17], v[38:41], v[144:147], v[2:17]
	ds_read_b128 v[34:37], v172 offset:1024
	ds_read_b128 v[38:41], v172 offset:1536
	s_waitcnt lgkmcnt(2)
	v_mfma_f32_32x32x16_f16 v[18:33], v[50:53], v[144:147], v[18:33]
	s_waitcnt lgkmcnt(1)
	v_mfma_f32_32x32x16_f16 v[2:17], v[34:37], v[140:143], v[2:17]
	ds_read_b128 v[34:37], v172 offset:9216
	ds_read_b128 v[42:45], v172 offset:9728
	s_waitcnt lgkmcnt(1)
	v_mfma_f32_32x32x16_f16 v[18:33], v[34:37], v[140:143], v[18:33]
	ds_read_b128 v[34:37], v174 offset:1024
	ds_read_b128 v[46:49], v174 offset:1536
	s_waitcnt lgkmcnt(1)
	v_mfma_f32_32x32x16_f16 v[2:17], v[34:37], v[136:139], v[2:17]
	ds_read_b128 v[34:37], v174 offset:9216
	ds_read_b128 v[50:53], v174 offset:9728
	v_mfma_f32_32x32x16_f16 v[2:17], v[38:41], v[132:135], v[2:17]
	s_waitcnt lgkmcnt(1)
	v_mfma_f32_32x32x16_f16 v[18:33], v[34:37], v[136:139], v[18:33]
	v_mov_b32_e32 v34, 0xf149f2ca
	v_mfma_f32_32x32x16_f16 v[2:17], v[46:49], v[128:131], v[2:17]
	v_mfma_f32_32x32x16_f16 v[18:33], v[42:45], v[132:135], v[18:33]
	s_nop 10
	v_max_f32_e32 v35, v3, v3
	v_max_f32_e32 v36, v2, v2
	v_max_f32_e32 v35, v36, v35
	v_max3_f32 v35, v35, v4, v5
	v_max3_f32 v35, v35, v6, v7
	v_max3_f32 v35, v35, v8, v9
	v_max3_f32 v35, v35, v10, v11
	s_waitcnt lgkmcnt(0)
	v_mfma_f32_32x32x16_f16 v[18:33], v[50:53], v[128:131], v[18:33]
	v_max3_f32 v35, v35, v12, v13
	v_max3_f32 v35, v35, v14, v15
	v_max3_f32 v35, v35, v16, v17
	s_nop 8
	v_max3_f32 v35, v35, v18, v19
	v_max3_f32 v35, v35, v20, v21
	v_max3_f32 v35, v35, v22, v23
	v_max3_f32 v35, v35, v24, v25
	v_max3_f32 v35, v35, v26, v27
	v_max3_f32 v35, v35, v28, v29
	v_max3_f32 v35, v35, v30, v31
	v_max3_f32 v35, v35, v32, v33
	v_mov_b32_e32 v36, v35
	s_nop 1
	v_permlane32_swap_b32_e32 v35, v36
	v_max_f32_e32 v36, v36, v36
	v_max_f32_e32 v35, v35, v35
	v_max_f32_e32 v35, v35, v36
	v_add_f32_e32 v36, 0x7149f2ca, v35
	v_cmp_ge_f32_e32 vcc, s33, v36
	s_cmp_eq_u64 vcc, exec
	v_max_f32_e32 v35, 0xf149f2ca, v35
	s_cselect_b64 vcc, -1, 0
	v_cndmask_b32_e32 v168, v35, v34, vcc
	v_sub_f32_e32 v96, v18, v168
	v_sub_f32_e32 v97, v19, v168
	v_lshlrev_b32_e32 v18, 4, v0
	v_lshrrev_b32_e32 v19, 4, v0
	v_sub_f32_e32 v98, v20, v168
	v_and_b32_e32 v18, 0xc0, v18
	v_bitop3_b32 v19, v19, v54, 1 bitop3:0x6c
	v_lshlrev_b32_e32 v20, 3, v0
	v_sub_f32_e32 v99, v21, v168
	v_lshl_or_b32 v18, v54, 11, v18
	v_lshlrev_b32_e32 v19, 5, v19
	v_and_b32_e32 v21, 8, v20
	v_or3_b32 v18, v18, v21, v19
	v_and_b32_e32 v19, 16, v20
	v_sub_f32_e32 v0, 0xf149f2ca, v35
	v_add3_u32 v163, v19, s37, v18
	v_bitop3_b32 v169, v18, s4, v19 bitop3:0x36
	v_exp_f32_e32 v18, v0
	s_add_u32 s2, s2, s20
	v_sub_f32_e32 v2, v2, v168
	v_sub_f32_e32 v3, v3, v168
	v_sub_f32_e32 v4, v4, v168
	v_sub_f32_e32 v5, v5, v168
	v_sub_f32_e32 v6, v6, v168
	v_sub_f32_e32 v7, v7, v168
	v_sub_f32_e32 v8, v8, v168
	v_sub_f32_e32 v9, v9, v168
	v_sub_f32_e32 v10, v10, v168
	v_sub_f32_e32 v11, v11, v168
	v_sub_f32_e32 v12, v12, v168
	v_sub_f32_e32 v13, v13, v168
	v_sub_f32_e32 v14, v14, v168
	v_sub_f32_e32 v15, v15, v168
	v_sub_f32_e32 v16, v16, v168
	v_sub_f32_e32 v17, v17, v168
	s_addc_u32 s3, s3, s21
	s_mov_b32 s4, s5
	v_exp_f32_e32 v127, v2
	v_exp_f32_e32 v180, v3
	v_exp_f32_e32 v125, v4
	v_exp_f32_e32 v179, v5
	v_exp_f32_e32 v123, v6
	v_exp_f32_e32 v126, v7
	v_exp_f32_e32 v122, v8
	v_exp_f32_e32 v124, v9
	v_exp_f32_e32 v119, v10
	v_exp_f32_e32 v121, v11
	v_exp_f32_e32 v117, v12
	v_exp_f32_e32 v120, v13
	v_exp_f32_e32 v115, v14
	v_exp_f32_e32 v118, v15
	v_exp_f32_e32 v114, v16
	v_exp_f32_e32 v116, v17
	v_or3_b32 v0, s2, v1, v164
	v_mov_b32_e32 v1, s3
	v_lshlrev_b32_e32 v164, 3, v54
	v_mov_b64_e32 v[62:63], s[18:19]
	v_lshl_add_u64 v[0:1], s[22:23], 0, v[0:1]
	s_mov_b64 s[2:3], 0xc080
	v_mov_b64_e32 v[48:49], s[4:5]
	v_sub_f32_e32 v100, v22, v168
	v_sub_f32_e32 v101, v23, v168
	v_sub_f32_e32 v102, v24, v168
	v_sub_f32_e32 v103, v25, v168
	v_sub_f32_e32 v104, v26, v168
	v_sub_f32_e32 v105, v27, v168
	v_sub_f32_e32 v106, v28, v168
	v_sub_f32_e32 v107, v29, v168
	v_sub_f32_e32 v108, v30, v168
	v_sub_f32_e32 v109, v31, v168
	v_sub_f32_e32 v110, v32, v168
	v_sub_f32_e32 v111, v33, v168
	v_lshl_add_u64 v[170:171], v[0:1], 0, s[2:3]
	s_movk_i32 s2, 0xbf80
	s_movk_i32 s20, 0xc000
	s_movk_i32 s22, 0xff80
	v_cndmask_b32_e64 v166, v18, 1.0, vcc
	v_mov_b64_e32 v[60:61], s[16:17]
	v_mov_b64_e32 v[58:59], s[14:15]
	v_mov_b64_e32 v[56:57], s[12:13]
	v_mov_b64_e32 v[54:55], s[10:11]
	v_mov_b64_e32 v[52:53], s[8:9]
	v_mov_b64_e32 v[50:51], s[6:7]
	v_mov_b64_e32 v[32:33], v[48:49]
	v_mov_b64_e32 v[16:17], v[48:49]
	v_mov_b64_e32 v[0:1], v[48:49]
	s_mov_b32 s3, -1
	s_mov_b32 s21, -1
	s_mov_b32 s23, -1
	v_add_u32_e32 v167, s37, v169
	v_mov_b64_e32 v[34:35], v[50:51]
	v_mov_b64_e32 v[36:37], v[52:53]
	v_mov_b64_e32 v[38:39], v[54:55]
	v_mov_b64_e32 v[40:41], v[56:57]
	v_mov_b64_e32 v[42:43], v[58:59]
	v_mov_b64_e32 v[44:45], v[60:61]
	v_mov_b64_e32 v[46:47], v[62:63]
	v_mov_b64_e32 v[18:19], v[50:51]
	v_mov_b64_e32 v[20:21], v[52:53]
	v_mov_b64_e32 v[22:23], v[54:55]
	v_mov_b64_e32 v[24:25], v[56:57]
	v_mov_b64_e32 v[26:27], v[58:59]
	v_mov_b64_e32 v[28:29], v[60:61]
	v_mov_b64_e32 v[30:31], v[62:63]
	v_mov_b64_e32 v[2:3], v[50:51]
	v_mov_b64_e32 v[4:5], v[52:53]
	v_mov_b64_e32 v[6:7], v[54:55]
	v_mov_b64_e32 v[8:9], v[56:57]
	v_mov_b64_e32 v[10:11], v[58:59]
	v_mov_b64_e32 v[12:13], v[60:61]
	v_mov_b64_e32 v[14:15], v[62:63]
.LBB1_1:
	s_lshl_b32 s6, s36, 14
	s_add_i32 s7, s6, 0
	s_waitcnt vmcnt(0)
	v_add_u32_e32 v112, s7, v175
	s_waitcnt lgkmcnt(0)
	s_barrier
	ds_read_b128 v[64:67], v112
	ds_read_b128 v[68:71], v112 offset:8192
	v_add_u32_e32 v113, s7, v176
	v_exp_f32_e32 v96, v96
	v_exp_f32_e32 v97, v97
	v_exp_f32_e32 v98, v98
	s_waitcnt lgkmcnt(1)
	v_mfma_f32_32x32x16_f16 v[80:95], v[64:67], v[156:159], 0
	ds_read_b128 v[182:185], v113
	ds_read_b128 v[186:189], v113 offset:8192
	v_exp_f32_e32 v99, v99
	v_exp_f32_e32 v181, v102
	v_exp_f32_e32 v218, v103
	v_exp_f32_e32 v219, v104
	v_exp_f32_e32 v220, v105
	s_waitcnt lgkmcnt(2)
	v_mfma_f32_32x32x16_f16 v[64:79], v[68:71], v[156:159], 0
	ds_read_b128 v[190:193], v112 offset:512
	ds_read_b128 v[194:197], v112 offset:8704
	v_exp_f32_e32 v221, v106
	v_exp_f32_e32 v222, v107
	v_exp_f32_e32 v223, v108
	v_exp_f32_e32 v224, v109
	v_exp_f32_e32 v225, v110
	s_waitcnt lgkmcnt(3)
	v_mfma_f32_32x32x16_f16 v[80:95], v[182:185], v[152:155], v[80:95]
	ds_read_b128 v[182:185], v113 offset:512
	ds_read_b128 v[198:201], v113 offset:8704
	v_exp_f32_e32 v226, v111
	v_cvt_pk_f16_f32 v102, v123, v126
	v_cvt_pk_f16_f32 v103, v122, v124
	v_cvt_pk_f16_f32 v104, v119, v121
	v_cvt_pk_f16_f32 v105, v117, v120
	s_waitcnt lgkmcnt(4)
	v_mfma_f32_32x32x16_f16 v[64:79], v[186:189], v[152:155], v[64:79]
	ds_read_b128 v[186:189], v112 offset:1024
	ds_read_b128 v[202:205], v112 offset:9216
	v_cvt_pk_f16_f32 v106, v115, v118
	v_cvt_pk_f16_f32 v107, v114, v116
	v_cvt_pk_f16_f32 v108, v96, v97
	v_cvt_pk_f16_f32 v109, v98, v99
	v_cvt_pk_f16_f32 v111, v181, v218
	s_waitcnt lgkmcnt(5)
	v_mfma_f32_32x32x16_f16 v[80:95], v[190:193], v[148:151], v[80:95]
	ds_read_b128 v[190:193], v113 offset:1024
	ds_read_b128 v[206:209], v113 offset:9216
	s_mov_b32 s4, s36
	v_permlane32_swap_b32_e32 v104, v106
	v_permlane32_swap_b32_e32 v105, v107
	s_waitcnt lgkmcnt(6)
	v_mfma_f32_32x32x16_f16 v[64:79], v[194:197], v[148:151], v[64:79]
	ds_read_b128 v[194:197], v112 offset:1536
	ds_read_b128 v[210:213], v112 offset:9728
	v_exp_f32_e32 v112, v100
	v_add_f32_e32 v100, 0, v127
	v_add_f32_e32 v100, v180, v100
	v_add_f32_e32 v100, v125, v100
	v_add_f32_e32 v100, v179, v100
	s_waitcnt lgkmcnt(7)
	v_mfma_f32_32x32x16_f16 v[80:95], v[182:185], v[144:147], v[80:95]
	ds_read_b128 v[182:185], v113 offset:1536
	ds_read_b128 v[214:217], v113 offset:9728
	v_add_f32_e32 v100, v123, v100
	v_add_f32_e32 v100, v126, v100
	v_add_f32_e32 v100, v122, v100
	v_add_f32_e32 v100, v124, v100
	v_add_f32_e32 v100, v119, v100
	s_waitcnt lgkmcnt(8)
	v_mfma_f32_32x32x16_f16 v[64:79], v[198:201], v[144:147], v[64:79]
	v_add_f32_e32 v100, v121, v100
	v_add_f32_e32 v100, v117, v100
	v_add_f32_e32 v100, v120, v100
	v_add_f32_e32 v100, v115, v100
	v_add_f32_e32 v100, v118, v100
	v_add_f32_e32 v100, v114, v100
	v_add_f32_e32 v100, v116, v100
	s_waitcnt lgkmcnt(7)
	v_mfma_f32_32x32x16_f16 v[80:95], v[186:189], v[140:143], v[80:95]
	v_add_f32_e32 v100, v96, v100
	v_exp_f32_e32 v113, v101
	v_add_f32_e32 v100, v97, v100
	v_add_f32_e32 v100, v98, v100
	v_add_f32_e32 v100, v99, v100
	v_add_f32_e32 v100, v112, v100
	v_add_f32_e32 v100, v113, v100
	s_waitcnt lgkmcnt(6)
	v_mfma_f32_32x32x16_f16 v[64:79], v[202:205], v[140:143], v[64:79]
	v_add_f32_e32 v100, v181, v100
	v_add_f32_e32 v100, v218, v100
	v_add_f32_e32 v100, v219, v100
	v_add_f32_e32 v100, v220, v100
	v_add_f32_e32 v100, v221, v100
	v_add_f32_e32 v100, v222, v100
	v_add_f32_e32 v100, v223, v100
	s_waitcnt lgkmcnt(5)
	v_mfma_f32_32x32x16_f16 v[80:95], v[190:193], v[136:139], v[80:95]
	v_add_f32_e32 v100, v224, v100
	v_add_f32_e32 v100, v225, v100
	v_add_f32_e32 v177, v226, v100
	v_mov_b32_e32 v178, v177
	v_cvt_pk_f16_f32 v100, v127, v180
	v_cvt_pk_f16_f32 v101, v125, v179
	v_cvt_pk_f16_f32 v110, v112, v113
	s_waitcnt lgkmcnt(4)
	v_mfma_f32_32x32x16_f16 v[64:79], v[206:209], v[136:139], v[64:79]
	v_cvt_pk_f16_f32 v96, v219, v220
	v_cvt_pk_f16_f32 v97, v221, v222
	v_cvt_pk_f16_f32 v98, v223, v224
	v_cvt_pk_f16_f32 v99, v225, v226
	v_permlane32_swap_b32_e32 v177, v178
	v_permlane32_swap_b32_e32 v100, v102
	s_waitcnt lgkmcnt(3)
	v_mfma_f32_32x32x16_f16 v[80:95], v[194:197], v[132:135], v[80:95]
	v_permlane32_swap_b32_e32 v101, v103
	v_permlane32_swap_b32_e32 v108, v110
	v_permlane32_swap_b32_e32 v109, v111
	v_permlane32_swap_b32_e32 v96, v98
	s_waitcnt lgkmcnt(2)
	v_mfma_f32_32x32x16_f16 v[64:79], v[210:213], v[132:135], v[64:79]
	v_permlane32_swap_b32_e32 v97, v99
	v_cmp_gt_f32_e32 vcc, 1.0, v166
	s_waitcnt lgkmcnt(1)
	v_mfma_f32_32x32x16_f16 v[80:95], v[182:185], v[128:131], v[80:95]
	s_waitcnt lgkmcnt(0)
	v_mfma_f32_32x32x16_f16 v[64:79], v[214:217], v[128:131], v[64:79]
	s_cbranch_vccz .LBB1_3
	v_pk_mul_f32 v[62:63], v[166:167], v[62:63] op_sel_hi:[0,1]
	v_pk_mul_f32 v[60:61], v[166:167], v[60:61] op_sel_hi:[0,1]
	v_pk_mul_f32 v[58:59], v[166:167], v[58:59] op_sel_hi:[0,1]
	v_pk_mul_f32 v[56:57], v[166:167], v[56:57] op_sel_hi:[0,1]
	v_pk_mul_f32 v[54:55], v[166:167], v[54:55] op_sel_hi:[0,1]
	v_pk_mul_f32 v[52:53], v[166:167], v[52:53] op_sel_hi:[0,1]
	v_pk_mul_f32 v[50:51], v[166:167], v[50:51] op_sel_hi:[0,1]
	v_pk_mul_f32 v[48:49], v[166:167], v[48:49] op_sel_hi:[0,1]
	v_pk_mul_f32 v[46:47], v[166:167], v[46:47] op_sel_hi:[0,1]
	v_pk_mul_f32 v[44:45], v[166:167], v[44:45] op_sel_hi:[0,1]
	v_pk_mul_f32 v[42:43], v[166:167], v[42:43] op_sel_hi:[0,1]
	v_pk_mul_f32 v[40:41], v[166:167], v[40:41] op_sel_hi:[0,1]
	v_pk_mul_f32 v[38:39], v[166:167], v[38:39] op_sel_hi:[0,1]
	v_pk_mul_f32 v[36:37], v[166:167], v[36:37] op_sel_hi:[0,1]
	v_pk_mul_f32 v[34:35], v[166:167], v[34:35] op_sel_hi:[0,1]
	v_pk_mul_f32 v[32:33], v[166:167], v[32:33] op_sel_hi:[0,1]
	v_pk_mul_f32 v[30:31], v[166:167], v[30:31] op_sel_hi:[0,1]
	v_pk_mul_f32 v[28:29], v[166:167], v[28:29] op_sel_hi:[0,1]
	v_pk_mul_f32 v[26:27], v[166:167], v[26:27] op_sel_hi:[0,1]
	v_pk_mul_f32 v[24:25], v[166:167], v[24:25] op_sel_hi:[0,1]
	v_pk_mul_f32 v[22:23], v[166:167], v[22:23] op_sel_hi:[0,1]
	v_pk_mul_f32 v[20:21], v[166:167], v[20:21] op_sel_hi:[0,1]
	v_pk_mul_f32 v[18:19], v[166:167], v[18:19] op_sel_hi:[0,1]
	v_pk_mul_f32 v[16:17], v[166:167], v[16:17] op_sel_hi:[0,1]
	v_pk_mul_f32 v[14:15], v[166:167], v[14:15] op_sel_hi:[0,1]
	v_pk_mul_f32 v[12:13], v[166:167], v[12:13] op_sel_hi:[0,1]
	v_pk_mul_f32 v[10:11], v[166:167], v[10:11] op_sel_hi:[0,1]
	v_pk_mul_f32 v[8:9], v[166:167], v[8:9] op_sel_hi:[0,1]
	v_pk_mul_f32 v[6:7], v[166:167], v[6:7] op_sel_hi:[0,1]
	v_pk_mul_f32 v[4:5], v[166:167], v[4:5] op_sel_hi:[0,1]
	v_pk_mul_f32 v[2:3], v[166:167], v[2:3] op_sel_hi:[0,1]
	v_pk_mul_f32 v[0:1], v[166:167], v[0:1] op_sel_hi:[0,1]
.LBB1_3:
	s_lshl_b32 s8, s35, 14
	v_add_u32_e32 v114, s8, v173
	v_lshl_add_u64 v[112:113], v[170:171], 0, s[2:3]
	v_readfirstlane_b32 s7, v114
	v_add_u32_e32 v114, 0x400, v114
	s_mov_b32 m0, s7
	v_readfirstlane_b32 s7, v114
	global_load_lds_dwordx4 v[112:113], off
	v_lshl_add_u64 v[112:113], v[170:171], 0, s[20:21]
	s_mov_b32 m0, s7
	s_lshl_b32 s7, s5, 14
	global_load_lds_dwordx4 v[112:113], off
	v_add_u32_e32 v179, s7, v163
	ds_read_b64_tr_b16 v[112:113], v179 offset:0
	v_add_u32_e32 v200, s7, v167
	ds_read_b64_tr_b16 v[114:115], v200 offset:0
	ds_read_b64_tr_b16 v[116:117], v179 offset:0x1000
	ds_read_b64_tr_b16 v[118:119], v200 offset:0x1000
	ds_read_b64_tr_b16 v[120:121], v179 offset:0x2000
	ds_read_b64_tr_b16 v[122:123], v200 offset:0x2000
	ds_read_b64_tr_b16 v[124:125], v179 offset:0x3000
	ds_read_b64_tr_b16 v[126:127], v200 offset:0x3000
	ds_read_b64_tr_b16 v[180:181], v179 offset:0x200
	ds_read_b64_tr_b16 v[182:183], v200 offset:0x200
	ds_read_b64_tr_b16 v[184:185], v179 offset:0x1200
	ds_read_b64_tr_b16 v[186:187], v200 offset:0x1200
	ds_read_b64_tr_b16 v[188:189], v179 offset:0x2200
	ds_read_b64_tr_b16 v[190:191], v200 offset:0x2200
	ds_read_b64_tr_b16 v[192:193], v179 offset:0x3200
	ds_read_b64_tr_b16 v[194:195], v200 offset:0x3200
	s_nop 0
	s_waitcnt lgkmcnt(14)
	v_mfma_f32_32x32x16_f16 v[48:63], v[112:115], v[100:103], v[48:63]
	ds_read_b64_tr_b16 v[112:113], v179 offset:0x400
	ds_read_b64_tr_b16 v[114:115], v200 offset:0x400
	s_waitcnt lgkmcnt(8)
	v_mfma_f32_32x32x16_f16 v[32:47], v[180:183], v[100:103], v[32:47]
	v_mfma_f32_32x32x16_f16 v[48:63], v[116:119], v[104:107], v[48:63]
	ds_read_b64_tr_b16 v[116:117], v179 offset:0x1400
	ds_read_b64_tr_b16 v[118:119], v200 offset:0x1400
	s_waitcnt lgkmcnt(8)
	v_mfma_f32_32x32x16_f16 v[32:47], v[184:187], v[104:107], v[32:47]
	v_mfma_f32_32x32x16_f16 v[48:63], v[120:123], v[108:111], v[48:63]
	ds_read_b64_tr_b16 v[120:121], v179 offset:0x2400
	ds_read_b64_tr_b16 v[122:123], v200 offset:0x2400
	ds_read_b64_tr_b16 v[180:181], v179 offset:0x3400
	ds_read_b64_tr_b16 v[182:183], v200 offset:0x3400
	ds_read_b64_tr_b16 v[184:185], v179 offset:0x600
	ds_read_b64_tr_b16 v[186:187], v200 offset:0x600
	s_waitcnt lgkmcnt(12)
	v_mfma_f32_32x32x16_f16 v[32:47], v[188:191], v[108:111], v[32:47]
	v_mfma_f32_32x32x16_f16 v[48:63], v[124:127], v[96:99], v[48:63]
	ds_read_b64_tr_b16 v[124:125], v179 offset:0x1600
	ds_read_b64_tr_b16 v[126:127], v200 offset:0x1600
	ds_read_b64_tr_b16 v[188:189], v179 offset:0x2600
	ds_read_b64_tr_b16 v[190:191], v200 offset:0x2600
	ds_read_b64_tr_b16 v[196:197], v179 offset:0x3600
	ds_read_b64_tr_b16 v[198:199], v200 offset:0x3600
	s_waitcnt lgkmcnt(15)
	v_mfma_f32_32x32x16_f16 v[32:47], v[192:195], v[96:99], v[32:47]
	v_max_f32_e32 v179, v81, v81
	v_max_f32_e32 v192, v80, v80
	v_max_f32_e32 v179, v192, v179
	v_max3_f32 v179, v179, v82, v83
	v_max3_f32 v179, v179, v84, v85
	v_max3_f32 v179, v179, v86, v87
	s_waitcnt lgkmcnt(14)
	v_mfma_f32_32x32x16_f16 v[16:31], v[112:115], v[100:103], v[16:31]
	v_max3_f32 v112, v179, v88, v89
	v_max3_f32 v112, v112, v90, v91
	v_max3_f32 v112, v112, v92, v93
	v_max3_f32 v112, v112, v94, v95
	v_max3_f32 v112, v112, v64, v65
	v_max3_f32 v112, v112, v66, v67
	v_max3_f32 v112, v112, v68, v69
	v_max3_f32 v112, v112, v70, v71
	v_max3_f32 v112, v112, v72, v73
	v_max3_f32 v112, v112, v74, v75
	v_max3_f32 v112, v112, v76, v77
	v_max3_f32 v112, v112, v78, v79
	v_mov_b32_e32 v113, v112
	s_nop 1
	v_permlane32_swap_b32_e32 v112, v113
	v_max_f32_e32 v113, v113, v113
	v_max_f32_e32 v112, v112, v112
	v_max_f32_e32 v179, v112, v113
	v_sub_f32_e32 v112, v179, v168
	v_cmp_ge_f32_e32 vcc, s33, v112
	s_cmp_eq_u64 vcc, exec
	s_cselect_b64 vcc, -1, 0
	s_add_i32 s8, s8, 0
	s_waitcnt vmcnt(0)
	v_add_u32_e32 v232, s8, v175
	s_waitcnt lgkmcnt(0)
	s_barrier
	ds_read_b128 v[112:115], v232
	ds_read_b128 v[192:195], v232 offset:8192
	v_mfma_f32_32x32x16_f16 v[0:15], v[184:187], v[100:103], v[0:15]
	v_add_u32_e32 v100, s8, v176
	ds_read_b128 v[184:187], v100
	ds_read_b128 v[200:203], v100 offset:8192
	v_max_f32_e32 v101, v168, v168
	v_max_f32_e32 v101, v101, v179
	v_sub_f32_e32 v102, v168, v101
	v_exp_f32_e32 v102, v102
	v_mfma_f32_32x32x16_f16 v[16:31], v[116:119], v[104:107], v[16:31]
	ds_read_b128 v[204:207], v232 offset:512
	ds_read_b128 v[208:211], v232 offset:8704
	v_cndmask_b32_e32 v179, v101, v168, vcc
	v_cndmask_b32_e64 v168, v102, 1.0, vcc
	v_sub_f32_e32 v80, v80, v179
	v_sub_f32_e32 v81, v81, v179
	v_sub_f32_e32 v82, v82, v179
	v_mfma_f32_32x32x16_f16 v[0:15], v[124:127], v[104:107], v[0:15]
	ds_read_b128 v[212:215], v100 offset:512
	ds_read_b128 v[216:219], v100 offset:8704
	v_sub_f32_e32 v83, v83, v179
	v_exp_f32_e32 v82, v82
	v_sub_f32_e32 v84, v84, v179
	v_sub_f32_e32 v68, v68, v179
	v_exp_f32_e32 v83, v83
	v_mfma_f32_32x32x16_f16 v[16:31], v[120:123], v[108:111], v[16:31]
	ds_read_b128 v[220:223], v232 offset:1024
	ds_read_b128 v[224:227], v232 offset:9216
	v_sub_f32_e32 v85, v85, v179
	v_exp_f32_e32 v84, v84
	v_sub_f32_e32 v86, v86, v179
	v_exp_f32_e32 v85, v85
	v_sub_f32_e32 v87, v87, v179
	v_mfma_f32_32x32x16_f16 v[0:15], v[188:191], v[108:111], v[0:15]
	ds_read_b128 v[188:191], v100 offset:1024
	ds_read_b128 v[228:231], v100 offset:9216
	v_exp_f32_e32 v86, v86
	v_sub_f32_e32 v88, v88, v179
	v_exp_f32_e32 v87, v87
	v_sub_f32_e32 v89, v89, v179
	v_exp_f32_e32 v88, v88
	v_mfma_f32_32x32x16_f16 v[16:31], v[180:183], v[96:99], v[16:31]
	ds_read_b128 v[180:183], v232 offset:1536
	ds_read_b128 v[232:235], v232 offset:9728
	v_sub_f32_e32 v90, v90, v179
	v_exp_f32_e32 v89, v89
	v_sub_f32_e32 v91, v91, v179
	v_exp_f32_e32 v90, v90
	v_sub_f32_e32 v92, v92, v179
	v_mfma_f32_32x32x16_f16 v[0:15], v[196:199], v[96:99], v[0:15]
	ds_read_b128 v[196:199], v100 offset:1536
	ds_read_b128 v[236:239], v100 offset:9728
	v_exp_f32_e32 v91, v91
	v_sub_f32_e32 v93, v93, v179
	v_exp_f32_e32 v92, v92
	v_sub_f32_e32 v94, v94, v179
	v_exp_f32_e32 v93, v93
	s_waitcnt lgkmcnt(15)
	v_mfma_f32_32x32x16_f16 v[112:127], v[112:115], v[156:159], 0
	v_sub_f32_e32 v95, v95, v179
	v_exp_f32_e32 v94, v94
	v_sub_f32_e32 v64, v64, v179
	v_exp_f32_e32 v95, v95
	v_sub_f32_e32 v65, v65, v179
	v_exp_f32_e32 v64, v64
	v_sub_f32_e32 v66, v66, v179
	s_waitcnt lgkmcnt(14)
	v_mfma_f32_32x32x16_f16 v[96:111], v[192:195], v[156:159], 0
	v_exp_f32_e32 v65, v65
	v_sub_f32_e32 v67, v67, v179
	v_exp_f32_e32 v66, v66
	v_exp_f32_e32 v67, v67
	v_sub_f32_e32 v69, v69, v179
	v_sub_f32_e32 v70, v70, v179
	v_sub_f32_e32 v71, v71, v179
	s_waitcnt lgkmcnt(13)
	v_mfma_f32_32x32x16_f16 v[112:127], v[184:187], v[152:155], v[112:127]
	v_exp_f32_e32 v184, v80
	v_exp_f32_e32 v185, v81
	v_exp_f32_e32 v186, v68
	v_exp_f32_e32 v187, v69
	v_add_f32_e32 v68, 0, v184
	v_add_f32_e32 v68, v185, v68
	v_add_f32_e32 v68, v82, v68
	s_waitcnt lgkmcnt(12)
	v_mfma_f32_32x32x16_f16 v[96:111], v[200:203], v[152:155], v[96:111]
	v_add_f32_e32 v68, v83, v68
	v_add_f32_e32 v68, v84, v68
	v_add_f32_e32 v68, v85, v68
	v_add_f32_e32 v68, v86, v68
	v_add_f32_e32 v68, v87, v68
	v_add_f32_e32 v68, v88, v68
	v_add_f32_e32 v68, v89, v68
	s_waitcnt lgkmcnt(11)
	v_mfma_f32_32x32x16_f16 v[112:127], v[204:207], v[148:151], v[112:127]
	v_add_f32_e32 v68, v90, v68
	v_add_f32_e32 v68, v91, v68
	v_add_f32_e32 v68, v92, v68
	v_add_f32_e32 v68, v93, v68
	v_add_f32_e32 v68, v94, v68
	v_add_f32_e32 v68, v95, v68
	v_add_f32_e32 v68, v64, v68
	s_waitcnt lgkmcnt(10)
	v_mfma_f32_32x32x16_f16 v[96:111], v[208:211], v[148:151], v[96:111]
	v_add_f32_e32 v68, v65, v68
	v_exp_f32_e32 v192, v70
	v_add_f32_e32 v68, v66, v68
	v_sub_f32_e32 v72, v72, v179
	v_exp_f32_e32 v71, v71
	v_add_f32_e32 v68, v67, v68
	v_sub_f32_e32 v73, v73, v179
	s_waitcnt lgkmcnt(9)
	v_mfma_f32_32x32x16_f16 v[112:127], v[212:215], v[144:147], v[112:127]
	v_exp_f32_e32 v193, v72
	v_add_f32_e32 v68, v186, v68
	v_sub_f32_e32 v74, v74, v179
	v_exp_f32_e32 v194, v73
	v_add_f32_e32 v68, v187, v68
	v_sub_f32_e32 v75, v75, v179
	v_exp_f32_e32 v195, v74
	s_waitcnt lgkmcnt(8)
	v_mfma_f32_32x32x16_f16 v[96:111], v[216:219], v[144:147], v[96:111]
	v_add_f32_e32 v68, v192, v68
	v_sub_f32_e32 v76, v76, v179
	v_exp_f32_e32 v200, v75
	v_add_f32_e32 v68, v71, v68
	v_sub_f32_e32 v77, v77, v179
	v_exp_f32_e32 v201, v76
	v_add_f32_e32 v68, v193, v68
	s_waitcnt lgkmcnt(7)
	v_mfma_f32_32x32x16_f16 v[112:127], v[220:223], v[140:143], v[112:127]
	v_sub_f32_e32 v78, v78, v179
	v_exp_f32_e32 v202, v77
	v_add_f32_e32 v68, v194, v68
	v_sub_f32_e32 v79, v79, v179
	v_exp_f32_e32 v203, v78
	v_add_f32_e32 v68, v195, v68
	v_exp_f32_e32 v204, v79
	s_waitcnt lgkmcnt(6)
	v_mfma_f32_32x32x16_f16 v[96:111], v[224:227], v[140:143], v[96:111]
	v_add_f32_e32 v68, v200, v68
	v_add_f32_e32 v68, v201, v68
	v_add_f32_e32 v68, v202, v68
	v_add_f32_e32 v68, v203, v68
	v_add_f32_e32 v80, v204, v68
	v_mov_b32_e32 v81, v80
	v_cvt_pk_f16_f32 v76, v184, v185
	s_waitcnt lgkmcnt(5)
	v_mfma_f32_32x32x16_f16 v[112:127], v[188:191], v[136:139], v[112:127]
	v_cvt_pk_f16_f32 v77, v82, v83
	v_cvt_pk_f16_f32 v78, v84, v85
	v_cvt_pk_f16_f32 v79, v86, v87
	v_cvt_pk_f16_f32 v72, v88, v89
	v_cvt_pk_f16_f32 v73, v90, v91
	v_cvt_pk_f16_f32 v74, v92, v93
	v_cvt_pk_f16_f32 v75, v94, v95
	s_waitcnt lgkmcnt(4)
	v_mfma_f32_32x32x16_f16 v[96:111], v[228:231], v[136:139], v[96:111]
	v_cvt_pk_f16_f32 v68, v64, v65
	v_cvt_pk_f16_f32 v69, v66, v67
	v_cvt_pk_f16_f32 v70, v186, v187
	v_cvt_pk_f16_f32 v71, v192, v71
	v_cvt_pk_f16_f32 v64, v193, v194
	v_cvt_pk_f16_f32 v65, v195, v200
	v_cvt_pk_f16_f32 v66, v201, v202
	s_waitcnt lgkmcnt(3)
	v_mfma_f32_32x32x16_f16 v[112:127], v[180:183], v[132:135], v[112:127]
	v_cvt_pk_f16_f32 v67, v203, v204
	v_permlane32_swap_b32_e32 v80, v81
	v_permlane32_swap_b32_e32 v76, v78
	v_permlane32_swap_b32_e32 v77, v79
	s_waitcnt lgkmcnt(2)
	v_mfma_f32_32x32x16_f16 v[96:111], v[232:235], v[132:135], v[96:111]
	v_permlane32_swap_b32_e32 v72, v74
	v_permlane32_swap_b32_e32 v73, v75
	v_permlane32_swap_b32_e32 v68, v70
	v_permlane32_swap_b32_e32 v69, v71
	s_waitcnt lgkmcnt(1)
	v_mfma_f32_32x32x16_f16 v[112:127], v[196:199], v[128:131], v[112:127]
	v_permlane32_swap_b32_e32 v64, v66
	v_permlane32_swap_b32_e32 v65, v67
	v_cmp_gt_f32_e32 vcc, 1.0, v168
	s_waitcnt lgkmcnt(0)
	v_mfma_f32_32x32x16_f16 v[96:111], v[236:239], v[128:131], v[96:111]
	s_cbranch_vccz .LBB1_5
	v_pk_mul_f32 v[62:63], v[168:169], v[62:63] op_sel_hi:[0,1]
	v_pk_mul_f32 v[60:61], v[168:169], v[60:61] op_sel_hi:[0,1]
	v_pk_mul_f32 v[58:59], v[168:169], v[58:59] op_sel_hi:[0,1]
	v_pk_mul_f32 v[56:57], v[168:169], v[56:57] op_sel_hi:[0,1]
	v_pk_mul_f32 v[54:55], v[168:169], v[54:55] op_sel_hi:[0,1]
	v_pk_mul_f32 v[52:53], v[168:169], v[52:53] op_sel_hi:[0,1]
	v_pk_mul_f32 v[50:51], v[168:169], v[50:51] op_sel_hi:[0,1]
	v_pk_mul_f32 v[48:49], v[168:169], v[48:49] op_sel_hi:[0,1]
	v_pk_mul_f32 v[46:47], v[168:169], v[46:47] op_sel_hi:[0,1]
	v_pk_mul_f32 v[44:45], v[168:169], v[44:45] op_sel_hi:[0,1]
	v_pk_mul_f32 v[42:43], v[168:169], v[42:43] op_sel_hi:[0,1]
	v_pk_mul_f32 v[40:41], v[168:169], v[40:41] op_sel_hi:[0,1]
	v_pk_mul_f32 v[38:39], v[168:169], v[38:39] op_sel_hi:[0,1]
	v_pk_mul_f32 v[36:37], v[168:169], v[36:37] op_sel_hi:[0,1]
	v_pk_mul_f32 v[34:35], v[168:169], v[34:35] op_sel_hi:[0,1]
	v_pk_mul_f32 v[32:33], v[168:169], v[32:33] op_sel_hi:[0,1]
	v_pk_mul_f32 v[30:31], v[168:169], v[30:31] op_sel_hi:[0,1]
	v_pk_mul_f32 v[28:29], v[168:169], v[28:29] op_sel_hi:[0,1]
	v_pk_mul_f32 v[26:27], v[168:169], v[26:27] op_sel_hi:[0,1]
	v_pk_mul_f32 v[24:25], v[168:169], v[24:25] op_sel_hi:[0,1]
	v_pk_mul_f32 v[22:23], v[168:169], v[22:23] op_sel_hi:[0,1]
	v_pk_mul_f32 v[20:21], v[168:169], v[20:21] op_sel_hi:[0,1]
	v_pk_mul_f32 v[18:19], v[168:169], v[18:19] op_sel_hi:[0,1]
	v_pk_mul_f32 v[16:17], v[168:169], v[16:17] op_sel_hi:[0,1]
	v_pk_mul_f32 v[14:15], v[168:169], v[14:15] op_sel_hi:[0,1]
	v_pk_mul_f32 v[12:13], v[168:169], v[12:13] op_sel_hi:[0,1]
	v_pk_mul_f32 v[10:11], v[168:169], v[10:11] op_sel_hi:[0,1]
	v_pk_mul_f32 v[8:9], v[168:169], v[8:9] op_sel_hi:[0,1]
	v_pk_mul_f32 v[6:7], v[168:169], v[6:7] op_sel_hi:[0,1]
	v_pk_mul_f32 v[4:5], v[168:169], v[4:5] op_sel_hi:[0,1]
	v_pk_mul_f32 v[2:3], v[168:169], v[2:3] op_sel_hi:[0,1]
	v_pk_mul_f32 v[0:1], v[168:169], v[0:1] op_sel_hi:[0,1]
.LBB1_5:
	v_add_f32_e32 v82, v177, v178
	v_fmac_f32_e32 v82, v165, v166
	v_add_f32_e32 v165, v80, v81
	v_fmac_f32_e32 v165, v82, v168
	v_add_u32_e32 v82, s7, v173
	v_add_u32_e32 v83, 0x400, v82
	v_readfirstlane_b32 s7, v82
	v_lshl_add_u64 v[80:81], v[170:171], 0, s[22:23]
	s_mov_b32 m0, s7
	v_readfirstlane_b32 s7, v83
	global_load_lds_dwordx4 v[80:81], off
	s_mov_b32 m0, s7
	v_add_u32_e32 v166, s6, v163
	global_load_lds_dwordx4 v[170:171], off
	ds_read_b64_tr_b16 v[80:81], v166 offset:0
	v_add_u32_e32 v168, s6, v167
	ds_read_b64_tr_b16 v[82:83], v168 offset:0
	ds_read_b64_tr_b16 v[84:85], v166 offset:0x1000
	ds_read_b64_tr_b16 v[86:87], v168 offset:0x1000
	ds_read_b64_tr_b16 v[88:89], v166 offset:0x2000
	ds_read_b64_tr_b16 v[90:91], v168 offset:0x2000
	ds_read_b64_tr_b16 v[92:93], v166 offset:0x3000
	ds_read_b64_tr_b16 v[94:95], v168 offset:0x3000
	ds_read_b64_tr_b16 v[180:181], v166 offset:0x200
	ds_read_b64_tr_b16 v[182:183], v168 offset:0x200
	ds_read_b64_tr_b16 v[184:185], v166 offset:0x1200
	ds_read_b64_tr_b16 v[186:187], v168 offset:0x1200
	ds_read_b64_tr_b16 v[188:189], v166 offset:0x2200
	ds_read_b64_tr_b16 v[190:191], v168 offset:0x2200
	ds_read_b64_tr_b16 v[192:193], v166 offset:0x3200
	ds_read_b64_tr_b16 v[194:195], v168 offset:0x3200
	s_nop 0
	s_waitcnt lgkmcnt(14)
	v_mfma_f32_32x32x16_f16 v[48:63], v[80:83], v[76:79], v[48:63]
	ds_read_b64_tr_b16 v[80:81], v166 offset:0x400
	ds_read_b64_tr_b16 v[82:83], v168 offset:0x400
	s_waitcnt lgkmcnt(8)
	v_mfma_f32_32x32x16_f16 v[32:47], v[180:183], v[76:79], v[32:47]
	v_mfma_f32_32x32x16_f16 v[48:63], v[84:87], v[72:75], v[48:63]
	ds_read_b64_tr_b16 v[84:85], v166 offset:0x1400
	ds_read_b64_tr_b16 v[86:87], v168 offset:0x1400
	s_waitcnt lgkmcnt(8)
	v_mfma_f32_32x32x16_f16 v[32:47], v[184:187], v[72:75], v[32:47]
	v_mfma_f32_32x32x16_f16 v[48:63], v[88:91], v[68:71], v[48:63]
	ds_read_b64_tr_b16 v[88:89], v166 offset:0x2400
	ds_read_b64_tr_b16 v[90:91], v168 offset:0x2400
	ds_read_b64_tr_b16 v[180:181], v166 offset:0x3400
	ds_read_b64_tr_b16 v[182:183], v168 offset:0x3400
	ds_read_b64_tr_b16 v[184:185], v166 offset:0x600
	ds_read_b64_tr_b16 v[186:187], v168 offset:0x600
	s_waitcnt lgkmcnt(12)
	v_mfma_f32_32x32x16_f16 v[32:47], v[188:191], v[68:71], v[32:47]
	v_mfma_f32_32x32x16_f16 v[48:63], v[92:95], v[64:67], v[48:63]
	ds_read_b64_tr_b16 v[92:93], v166 offset:0x1600
	ds_read_b64_tr_b16 v[94:95], v168 offset:0x1600
	ds_read_b64_tr_b16 v[188:189], v166 offset:0x2600
	ds_read_b64_tr_b16 v[190:191], v168 offset:0x2600
	ds_read_b64_tr_b16 v[196:197], v166 offset:0x3600
	ds_read_b64_tr_b16 v[198:199], v168 offset:0x3600
	s_waitcnt lgkmcnt(15)
	v_mfma_f32_32x32x16_f16 v[32:47], v[192:195], v[64:67], v[32:47]
	v_max_f32_e32 v166, v113, v113
	v_max_f32_e32 v168, v112, v112
	v_max_f32_e32 v166, v168, v166
	v_max3_f32 v166, v166, v114, v115
	s_waitcnt lgkmcnt(14)
	v_mfma_f32_32x32x16_f16 v[16:31], v[80:83], v[76:79], v[16:31]
	v_max3_f32 v166, v166, v116, v117
	v_max3_f32 v80, v166, v118, v119
	v_max3_f32 v80, v80, v120, v121
	v_max3_f32 v80, v80, v122, v123
	v_max3_f32 v80, v80, v124, v125
	v_max3_f32 v80, v80, v126, v127
	v_max3_f32 v80, v80, v96, v97
	s_waitcnt lgkmcnt(6)
	v_mfma_f32_32x32x16_f16 v[0:15], v[184:187], v[76:79], v[0:15]
	v_max3_f32 v80, v80, v98, v99
	v_max3_f32 v76, v80, v100, v101
	v_max3_f32 v76, v76, v102, v103
	v_max3_f32 v76, v76, v104, v105
	v_max3_f32 v76, v76, v106, v107
	v_max3_f32 v76, v76, v108, v109
	v_max3_f32 v76, v76, v110, v111
	v_mfma_f32_32x32x16_f16 v[16:31], v[84:87], v[72:75], v[16:31]
	v_mov_b32_e32 v77, v76
	s_nop 1
	v_permlane32_swap_b32_e32 v76, v77
	v_max_f32_e32 v77, v77, v77
	v_max_f32_e32 v76, v76, v76
	v_max_f32_e32 v76, v76, v77
	v_sub_f32_e32 v77, v76, v179
	s_waitcnt lgkmcnt(4)
	v_mfma_f32_32x32x16_f16 v[0:15], v[92:95], v[72:75], v[0:15]
	v_cmp_ge_f32_e32 vcc, s33, v77
	v_max_f32_e32 v77, v179, v179
	v_max_f32_e32 v72, v77, v76
	v_sub_f32_e32 v73, v179, v72
	v_exp_f32_e32 v73, v73
	s_cmp_eq_u64 vcc, exec
	s_cselect_b64 vcc, -1, 0
	v_mfma_f32_32x32x16_f16 v[16:31], v[88:91], v[68:71], v[16:31]
	v_cndmask_b32_e32 v168, v72, v179, vcc
	v_cndmask_b32_e64 v166, v73, 1.0, vcc
	v_sub_f32_e32 v72, v112, v168
	v_sub_f32_e32 v73, v113, v168
	v_sub_f32_e32 v74, v114, v168
	v_sub_f32_e32 v75, v115, v168
	v_sub_f32_e32 v76, v116, v168
	s_waitcnt lgkmcnt(2)
	v_mfma_f32_32x32x16_f16 v[0:15], v[188:191], v[68:71], v[0:15]
	v_sub_f32_e32 v77, v117, v168
	v_sub_f32_e32 v78, v118, v168
	v_sub_f32_e32 v68, v119, v168
	v_sub_f32_e32 v69, v120, v168
	v_sub_f32_e32 v70, v121, v168
	v_sub_f32_e32 v71, v122, v168
	v_sub_f32_e32 v79, v123, v168
	v_mfma_f32_32x32x16_f16 v[16:31], v[180:183], v[64:67], v[16:31]
	v_sub_f32_e32 v80, v124, v168
	v_sub_f32_e32 v81, v125, v168
	v_sub_f32_e32 v82, v126, v168
	v_sub_f32_e32 v83, v127, v168
	v_exp_f32_e32 v127, v72
	v_exp_f32_e32 v180, v73
	v_exp_f32_e32 v125, v74
	s_waitcnt lgkmcnt(0)
	v_mfma_f32_32x32x16_f16 v[0:15], v[196:199], v[64:67], v[0:15]
	v_exp_f32_e32 v179, v75
	v_exp_f32_e32 v123, v76
	v_exp_f32_e32 v126, v77
	v_exp_f32_e32 v122, v78
	v_exp_f32_e32 v124, v68
	v_exp_f32_e32 v119, v69
	v_exp_f32_e32 v121, v70
	v_exp_f32_e32 v117, v71
	v_exp_f32_e32 v120, v79
	v_exp_f32_e32 v115, v80
	v_exp_f32_e32 v118, v81
	v_exp_f32_e32 v114, v82
	v_exp_f32_e32 v116, v83
	s_add_i32 s34, s34, 2
	v_sub_f32_e32 v96, v96, v168
	v_sub_f32_e32 v97, v97, v168
	v_sub_f32_e32 v98, v98, v168
	v_sub_f32_e32 v99, v99, v168
	v_sub_f32_e32 v100, v100, v168
	v_sub_f32_e32 v101, v101, v168
	v_sub_f32_e32 v102, v102, v168
	v_sub_f32_e32 v103, v103, v168
	v_sub_f32_e32 v104, v104, v168
	v_sub_f32_e32 v105, v105, v168
	v_sub_f32_e32 v106, v106, v168
	v_sub_f32_e32 v107, v107, v168
	v_sub_f32_e32 v108, v108, v168
	v_sub_f32_e32 v109, v109, v168
	v_sub_f32_e32 v110, v110, v168
	v_sub_f32_e32 v111, v111, v168
	s_cmp_gt_u32 s34, 12
	v_lshl_add_u64 v[170:171], v[170:171], 0, s[30:31]
	s_cbranch_scc1 .LBB1_7
	s_mov_b32 s36, s5
	s_mov_b32 s5, s35
	s_mov_b32 s35, s4
	s_branch .LBB1_1
.LBB1_7:
	s_waitcnt vmcnt(0)
	s_waitcnt lgkmcnt(0)
	s_barrier
	ds_read_b128 v[64:67], v172
	ds_read_b128 v[68:71], v172 offset:8192
	v_exp_f32_e32 v178, v100
	v_add_f32_e32 v100, 0, v127
	v_add_f32_e32 v100, v180, v100
	v_add_f32_e32 v100, v125, v100
	v_add_f32_e32 v100, v179, v100
	s_waitcnt lgkmcnt(1)
	v_mfma_f32_32x32x16_f16 v[80:95], v[64:67], v[156:159], 0
	ds_read_b128 v[182:185], v174
	ds_read_b128 v[186:189], v174 offset:8192
	v_add_f32_e32 v100, v123, v100
	v_add_f32_e32 v100, v126, v100
	v_add_f32_e32 v100, v122, v100
	v_add_f32_e32 v100, v124, v100
	v_add_f32_e32 v100, v119, v100
	s_waitcnt lgkmcnt(2)
	v_mfma_f32_32x32x16_f16 v[64:79], v[68:71], v[156:159], 0
	ds_read_b128 v[156:159], v172 offset:512
	ds_read_b128 v[190:193], v172 offset:8704
	v_add_f32_e32 v100, v121, v100
	v_add_f32_e32 v100, v117, v100
	v_add_f32_e32 v100, v120, v100
	v_exp_f32_e32 v96, v96
	v_add_f32_e32 v100, v115, v100
	s_waitcnt lgkmcnt(3)
	v_mfma_f32_32x32x16_f16 v[80:95], v[182:185], v[152:155], v[80:95]
	ds_read_b128 v[182:185], v174 offset:512
	ds_read_b128 v[194:197], v174 offset:8704
	v_exp_f32_e32 v97, v97
	v_add_f32_e32 v100, v118, v100
	v_exp_f32_e32 v98, v98
	v_add_f32_e32 v100, v114, v100
	v_exp_f32_e32 v99, v99
	s_waitcnt lgkmcnt(4)
	v_mfma_f32_32x32x16_f16 v[64:79], v[186:189], v[152:155], v[64:79]
	ds_read_b128 v[152:155], v172 offset:1024
	ds_read_b128 v[186:189], v172 offset:9216
	v_add_f32_e32 v100, v116, v100
	v_add_f32_e32 v100, v96, v100
	v_exp_f32_e32 v181, v101
	v_add_f32_e32 v100, v97, v100
	v_add_f32_e32 v100, v98, v100
	s_waitcnt lgkmcnt(5)
	v_mfma_f32_32x32x16_f16 v[80:95], v[156:159], v[148:151], v[80:95]
	ds_read_b128 v[156:159], v174 offset:1024
	ds_read_b128 v[198:201], v174 offset:9216
	v_add_f32_e32 v100, v99, v100
	v_add_f32_e32 v100, v178, v100
	v_add_f32_e32 v100, v181, v100
	v_exp_f32_e32 v202, v106
	v_exp_f32_e32 v203, v107
	s_waitcnt lgkmcnt(6)
	v_mfma_f32_32x32x16_f16 v[64:79], v[190:193], v[148:151], v[64:79]
	ds_read_b128 v[148:151], v172 offset:1536
	ds_read_b128 v[170:173], v172 offset:9728
	v_exp_f32_e32 v190, v102
	v_exp_f32_e32 v191, v103
	v_exp_f32_e32 v192, v104
	v_exp_f32_e32 v193, v105
	v_add_f32_e32 v100, v190, v100
	s_waitcnt lgkmcnt(7)
	v_mfma_f32_32x32x16_f16 v[80:95], v[182:185], v[144:147], v[80:95]
	ds_read_b128 v[182:185], v174 offset:1536
	ds_read_b128 v[174:177], v174 offset:9728
	v_add_f32_e32 v100, v191, v100
	v_exp_f32_e32 v204, v108
	v_add_f32_e32 v100, v192, v100
	v_exp_f32_e32 v205, v109
	v_add_f32_e32 v100, v193, v100
	s_waitcnt lgkmcnt(8)
	v_mfma_f32_32x32x16_f16 v[64:79], v[194:197], v[144:147], v[64:79]
	v_exp_f32_e32 v206, v110
	v_add_f32_e32 v100, v202, v100
	v_exp_f32_e32 v207, v111
	v_add_f32_e32 v100, v203, v100
	v_add_f32_e32 v100, v204, v100
	v_add_f32_e32 v100, v205, v100
	v_add_f32_e32 v100, v206, v100
	s_waitcnt lgkmcnt(7)
	v_mfma_f32_32x32x16_f16 v[80:95], v[152:155], v[140:143], v[80:95]
	v_add_f32_e32 v112, v207, v100
	v_mov_b32_e32 v113, v112
	v_cvt_pk_f16_f32 v100, v127, v180
	v_cvt_pk_f16_f32 v101, v125, v179
	v_cvt_pk_f16_f32 v102, v123, v126
	v_cvt_pk_f16_f32 v103, v122, v124
	v_cvt_pk_f16_f32 v108, v119, v121
	s_waitcnt lgkmcnt(6)
	v_mfma_f32_32x32x16_f16 v[64:79], v[186:189], v[140:143], v[64:79]
	v_cvt_pk_f16_f32 v109, v117, v120
	v_cvt_pk_f16_f32 v110, v115, v118
	v_cvt_pk_f16_f32 v111, v114, v116
	v_cvt_pk_f16_f32 v104, v96, v97
	v_cvt_pk_f16_f32 v105, v98, v99
	v_cvt_pk_f16_f32 v106, v178, v181
	v_cvt_pk_f16_f32 v107, v190, v191
	s_waitcnt lgkmcnt(5)
	v_mfma_f32_32x32x16_f16 v[80:95], v[156:159], v[136:139], v[80:95]
	v_cvt_pk_f16_f32 v96, v192, v193
	v_cvt_pk_f16_f32 v97, v202, v203
	v_cvt_pk_f16_f32 v98, v204, v205
	v_cvt_pk_f16_f32 v99, v206, v207
	v_permlane32_swap_b32_e32 v112, v113
	v_permlane32_swap_b32_e32 v100, v102
	s_waitcnt lgkmcnt(4)
	v_mfma_f32_32x32x16_f16 v[64:79], v[198:201], v[136:139], v[64:79]
	v_permlane32_swap_b32_e32 v101, v103
	v_permlane32_swap_b32_e32 v108, v110
	v_permlane32_swap_b32_e32 v109, v111
	v_permlane32_swap_b32_e32 v104, v106
	s_waitcnt lgkmcnt(3)
	v_mfma_f32_32x32x16_f16 v[80:95], v[148:151], v[132:135], v[80:95]
	v_permlane32_swap_b32_e32 v105, v107
	v_permlane32_swap_b32_e32 v96, v98
	v_permlane32_swap_b32_e32 v97, v99
	v_cmp_gt_f32_e32 vcc, 1.0, v166
	s_waitcnt lgkmcnt(2)
	v_mfma_f32_32x32x16_f16 v[64:79], v[170:173], v[132:135], v[64:79]
	s_waitcnt lgkmcnt(1)
	v_mfma_f32_32x32x16_f16 v[80:95], v[182:185], v[128:131], v[80:95]
	s_waitcnt lgkmcnt(0)
	v_mfma_f32_32x32x16_f16 v[64:79], v[174:177], v[128:131], v[64:79]
	s_cbranch_vccz .LBB1_9
	v_pk_mul_f32 v[62:63], v[166:167], v[62:63] op_sel_hi:[0,1]
	v_pk_mul_f32 v[60:61], v[166:167], v[60:61] op_sel_hi:[0,1]
	v_pk_mul_f32 v[58:59], v[166:167], v[58:59] op_sel_hi:[0,1]
	v_pk_mul_f32 v[56:57], v[166:167], v[56:57] op_sel_hi:[0,1]
	v_pk_mul_f32 v[54:55], v[166:167], v[54:55] op_sel_hi:[0,1]
	v_pk_mul_f32 v[52:53], v[166:167], v[52:53] op_sel_hi:[0,1]
	v_pk_mul_f32 v[50:51], v[166:167], v[50:51] op_sel_hi:[0,1]
	v_pk_mul_f32 v[48:49], v[166:167], v[48:49] op_sel_hi:[0,1]
	v_pk_mul_f32 v[46:47], v[166:167], v[46:47] op_sel_hi:[0,1]
	v_pk_mul_f32 v[44:45], v[166:167], v[44:45] op_sel_hi:[0,1]
	v_pk_mul_f32 v[42:43], v[166:167], v[42:43] op_sel_hi:[0,1]
	v_pk_mul_f32 v[40:41], v[166:167], v[40:41] op_sel_hi:[0,1]
	v_pk_mul_f32 v[38:39], v[166:167], v[38:39] op_sel_hi:[0,1]
	v_pk_mul_f32 v[36:37], v[166:167], v[36:37] op_sel_hi:[0,1]
	v_pk_mul_f32 v[34:35], v[166:167], v[34:35] op_sel_hi:[0,1]
	v_pk_mul_f32 v[32:33], v[166:167], v[32:33] op_sel_hi:[0,1]
	v_pk_mul_f32 v[30:31], v[166:167], v[30:31] op_sel_hi:[0,1]
	v_pk_mul_f32 v[28:29], v[166:167], v[28:29] op_sel_hi:[0,1]
	v_pk_mul_f32 v[26:27], v[166:167], v[26:27] op_sel_hi:[0,1]
	v_pk_mul_f32 v[24:25], v[166:167], v[24:25] op_sel_hi:[0,1]
	v_pk_mul_f32 v[22:23], v[166:167], v[22:23] op_sel_hi:[0,1]
	v_pk_mul_f32 v[20:21], v[166:167], v[20:21] op_sel_hi:[0,1]
	v_pk_mul_f32 v[18:19], v[166:167], v[18:19] op_sel_hi:[0,1]
	v_pk_mul_f32 v[16:17], v[166:167], v[16:17] op_sel_hi:[0,1]
	v_pk_mul_f32 v[14:15], v[166:167], v[14:15] op_sel_hi:[0,1]
	v_pk_mul_f32 v[12:13], v[166:167], v[12:13] op_sel_hi:[0,1]
	v_pk_mul_f32 v[10:11], v[166:167], v[10:11] op_sel_hi:[0,1]
	v_pk_mul_f32 v[8:9], v[166:167], v[8:9] op_sel_hi:[0,1]
	v_pk_mul_f32 v[6:7], v[166:167], v[6:7] op_sel_hi:[0,1]
	v_pk_mul_f32 v[4:5], v[166:167], v[4:5] op_sel_hi:[0,1]
	v_pk_mul_f32 v[2:3], v[166:167], v[2:3] op_sel_hi:[0,1]
	v_pk_mul_f32 v[0:1], v[166:167], v[0:1] op_sel_hi:[0,1]
.LBB1_9:
	s_cmp_lg_u32 0, -1
	s_cselect_b32 s2, 0, 0
	v_add_u32_e32 v148, 0x8000, v163
	s_add_i32 s2, s2, 0x8000
	ds_read_b64_tr_b16 v[114:115], v148 offset:0
	v_add_u32_e32 v150, s2, v169
	ds_read_b64_tr_b16 v[116:117], v150 offset:0
	ds_read_b64_tr_b16 v[118:119], v148 offset:0x1000
	ds_read_b64_tr_b16 v[120:121], v150 offset:0x1000
	ds_read_b64_tr_b16 v[122:123], v148 offset:0x2000
	ds_read_b64_tr_b16 v[124:125], v150 offset:0x2000
	ds_read_b64_tr_b16 v[126:127], v148 offset:0x3000
	ds_read_b64_tr_b16 v[128:129], v150 offset:0x3000
	ds_read_b64_tr_b16 v[130:131], v148 offset:0x200
	ds_read_b64_tr_b16 v[132:133], v150 offset:0x200
	ds_read_b64_tr_b16 v[134:135], v148 offset:0x1200
	ds_read_b64_tr_b16 v[136:137], v150 offset:0x1200
	ds_read_b64_tr_b16 v[138:139], v148 offset:0x2200
	ds_read_b64_tr_b16 v[140:141], v150 offset:0x2200
	ds_read_b64_tr_b16 v[142:143], v148 offset:0x3200
	ds_read_b64_tr_b16 v[144:145], v150 offset:0x3200
	s_nop 0
	s_waitcnt lgkmcnt(14)
	v_mfma_f32_32x32x16_f16 v[48:63], v[114:117], v[100:103], v[48:63]
	ds_read_b64_tr_b16 v[114:115], v148 offset:0x400
	ds_read_b64_tr_b16 v[116:117], v150 offset:0x400
	s_waitcnt lgkmcnt(8)
	v_mfma_f32_32x32x16_f16 v[32:47], v[130:133], v[100:103], v[32:47]
	v_mfma_f32_32x32x16_f16 v[48:63], v[118:121], v[108:111], v[48:63]
	ds_read_b64_tr_b16 v[118:119], v148 offset:0x1400
	ds_read_b64_tr_b16 v[120:121], v150 offset:0x1400
	s_waitcnt lgkmcnt(8)
	v_mfma_f32_32x32x16_f16 v[32:47], v[134:137], v[108:111], v[32:47]
	v_mfma_f32_32x32x16_f16 v[48:63], v[122:125], v[104:107], v[48:63]
	ds_read_b64_tr_b16 v[122:123], v148 offset:0x2400
	ds_read_b64_tr_b16 v[124:125], v150 offset:0x2400
	ds_read_b64_tr_b16 v[130:131], v148 offset:0x3400
	ds_read_b64_tr_b16 v[132:133], v150 offset:0x3400
	ds_read_b64_tr_b16 v[134:135], v148 offset:0x600
	ds_read_b64_tr_b16 v[136:137], v150 offset:0x600
	s_waitcnt lgkmcnt(12)
	v_mfma_f32_32x32x16_f16 v[32:47], v[138:141], v[104:107], v[32:47]
	v_mfma_f32_32x32x16_f16 v[48:63], v[126:129], v[96:99], v[48:63]
	ds_read_b64_tr_b16 v[126:127], v148 offset:0x1600
	ds_read_b64_tr_b16 v[128:129], v150 offset:0x1600
	ds_read_b64_tr_b16 v[138:139], v148 offset:0x2600
	ds_read_b64_tr_b16 v[140:141], v150 offset:0x2600
	ds_read_b64_tr_b16 v[146:147], v148 offset:0x3600
	ds_read_b64_tr_b16 v[148:149], v150 offset:0x3600
	s_waitcnt lgkmcnt(15)
	v_mfma_f32_32x32x16_f16 v[32:47], v[142:145], v[96:99], v[32:47]
	v_max_f32_e32 v142, v81, v81
	v_max_f32_e32 v143, v80, v80
	v_max_f32_e32 v142, v143, v142
	v_max3_f32 v142, v142, v82, v83
	v_max3_f32 v142, v142, v84, v85
	s_waitcnt lgkmcnt(14)
	v_mfma_f32_32x32x16_f16 v[16:31], v[114:117], v[100:103], v[16:31]
	v_max3_f32 v114, v142, v86, v87
	v_max3_f32 v114, v114, v88, v89
	v_max3_f32 v114, v114, v90, v91
	v_max3_f32 v114, v114, v92, v93
	v_max3_f32 v114, v114, v94, v95
	v_max3_f32 v114, v114, v64, v65
	v_max3_f32 v114, v114, v66, v67
	s_waitcnt lgkmcnt(6)
	v_mfma_f32_32x32x16_f16 v[0:15], v[134:137], v[100:103], v[0:15]
	v_max3_f32 v100, v114, v68, v69
	v_max3_f32 v100, v100, v70, v71
	v_max3_f32 v100, v100, v72, v73
	v_max3_f32 v100, v100, v74, v75
	v_max3_f32 v100, v100, v76, v77
	v_max3_f32 v100, v100, v78, v79
	v_mov_b32_e32 v101, v100
	v_mfma_f32_32x32x16_f16 v[16:31], v[118:121], v[108:111], v[16:31]
	s_nop 0
	v_permlane32_swap_b32_e32 v100, v101
	v_max_f32_e32 v101, v101, v101
	v_max_f32_e32 v100, v100, v100
	v_max_f32_e32 v100, v100, v101
	v_sub_f32_e32 v101, v100, v168
	s_mov_b32 s2, 0x41200000
	s_waitcnt lgkmcnt(4)
	v_mfma_f32_32x32x16_f16 v[0:15], v[126:129], v[108:111], v[0:15]
	v_cmp_ge_f32_e32 vcc, s2, v101
	s_cmp_eq_u64 vcc, exec
	v_max_f32_e32 v101, v168, v168
	v_max_f32_e32 v100, v101, v100
	s_cselect_b64 vcc, -1, 0
	v_sub_f32_e32 v101, v168, v100
	v_cndmask_b32_e32 v100, v100, v168, vcc
	v_mfma_f32_32x32x16_f16 v[16:31], v[122:125], v[104:107], v[16:31]
	v_sub_f32_e32 v80, v80, v100
	v_sub_f32_e32 v81, v81, v100
	v_sub_f32_e32 v82, v82, v100
	v_sub_f32_e32 v83, v83, v100
	v_exp_f32_e32 v82, v82
	v_sub_f32_e32 v84, v84, v100
	v_sub_f32_e32 v68, v68, v100
	s_waitcnt lgkmcnt(2)
	v_mfma_f32_32x32x16_f16 v[0:15], v[138:141], v[104:107], v[0:15]
	v_exp_f32_e32 v83, v83
	v_sub_f32_e32 v85, v85, v100
	v_exp_f32_e32 v84, v84
	v_sub_f32_e32 v86, v86, v100
	v_exp_f32_e32 v85, v85
	v_sub_f32_e32 v87, v87, v100
	v_exp_f32_e32 v86, v86
	v_mfma_f32_32x32x16_f16 v[16:31], v[130:133], v[96:99], v[16:31]
	v_sub_f32_e32 v88, v88, v100
	v_exp_f32_e32 v87, v87
	v_sub_f32_e32 v89, v89, v100
	v_exp_f32_e32 v88, v88
	v_sub_f32_e32 v90, v90, v100
	v_exp_f32_e32 v89, v89
	v_sub_f32_e32 v91, v91, v100
	s_waitcnt lgkmcnt(0)
	v_mfma_f32_32x32x16_f16 v[0:15], v[146:149], v[96:99], v[0:15]
	v_exp_f32_e32 v96, v80
	v_exp_f32_e32 v97, v81
	v_exp_f32_e32 v98, v68
	v_exp_f32_e32 v90, v90
	v_add_f32_e32 v68, 0, v96
	v_add_f32_e32 v68, v97, v68
	v_add_f32_e32 v68, v82, v68
	v_add_f32_e32 v68, v83, v68
	v_add_f32_e32 v68, v84, v68
	v_add_f32_e32 v68, v85, v68
	v_add_f32_e32 v68, v86, v68
	v_sub_f32_e32 v92, v92, v100
	v_exp_f32_e32 v91, v91
	v_add_f32_e32 v68, v87, v68
	v_sub_f32_e32 v93, v93, v100
	v_exp_f32_e32 v92, v92
	v_add_f32_e32 v68, v88, v68
	v_sub_f32_e32 v94, v94, v100
	v_exp_f32_e32 v93, v93
	v_add_f32_e32 v68, v89, v68
	v_sub_f32_e32 v95, v95, v100
	v_exp_f32_e32 v94, v94
	v_add_f32_e32 v68, v90, v68
	v_sub_f32_e32 v64, v64, v100
	v_exp_f32_e32 v95, v95
	v_add_f32_e32 v68, v91, v68
	v_sub_f32_e32 v65, v65, v100
	v_exp_f32_e32 v64, v64
	v_add_f32_e32 v68, v92, v68
	v_sub_f32_e32 v66, v66, v100
	v_exp_f32_e32 v65, v65
	v_add_f32_e32 v68, v93, v68
	v_exp_f32_e32 v101, v101
	v_sub_f32_e32 v67, v67, v100
	v_exp_f32_e32 v66, v66
	v_add_f32_e32 v68, v94, v68
	v_exp_f32_e32 v67, v67
	v_add_f32_e32 v68, v95, v68
	v_sub_f32_e32 v69, v69, v100
	v_add_f32_e32 v68, v64, v68
	v_sub_f32_e32 v70, v70, v100
	v_exp_f32_e32 v99, v69
	v_add_f32_e32 v68, v65, v68
	v_cndmask_b32_e64 v102, v101, 1.0, vcc
	v_sub_f32_e32 v71, v71, v100
	v_exp_f32_e32 v101, v70
	v_add_f32_e32 v68, v66, v68
	v_sub_f32_e32 v72, v72, v100
	v_exp_f32_e32 v71, v71
	v_add_f32_e32 v68, v67, v68
	v_sub_f32_e32 v73, v73, v100
	v_exp_f32_e32 v103, v72
	v_add_f32_e32 v68, v98, v68
	v_sub_f32_e32 v74, v74, v100
	v_exp_f32_e32 v104, v73
	v_add_f32_e32 v68, v99, v68
	v_sub_f32_e32 v75, v75, v100
	v_exp_f32_e32 v105, v74
	v_add_f32_e32 v68, v101, v68
	v_sub_f32_e32 v76, v76, v100
	v_exp_f32_e32 v106, v75
	v_add_f32_e32 v68, v71, v68
	v_sub_f32_e32 v77, v77, v100
	v_exp_f32_e32 v107, v76
	v_add_f32_e32 v68, v103, v68
	v_sub_f32_e32 v78, v78, v100
	v_exp_f32_e32 v108, v77
	v_add_f32_e32 v68, v104, v68
	v_sub_f32_e32 v79, v79, v100
	v_exp_f32_e32 v109, v78
	v_add_f32_e32 v68, v105, v68
	v_exp_f32_e32 v110, v79
	v_add_f32_e32 v68, v106, v68
	v_add_f32_e32 v68, v107, v68
	v_add_f32_e32 v68, v108, v68
	v_add_f32_e32 v68, v109, v68
	v_add_f32_e32 v80, v110, v68
	v_mov_b32_e32 v81, v80
	v_cvt_pk_f16_f32 v76, v96, v97
	v_cvt_pk_f16_f32 v77, v82, v83
	v_cvt_pk_f16_f32 v78, v84, v85
	v_cvt_pk_f16_f32 v79, v86, v87
	v_cvt_pk_f16_f32 v72, v88, v89
	v_cvt_pk_f16_f32 v73, v90, v91
	v_cvt_pk_f16_f32 v74, v92, v93
	v_cvt_pk_f16_f32 v75, v94, v95
	v_cvt_pk_f16_f32 v68, v64, v65
	v_cvt_pk_f16_f32 v69, v66, v67
	v_cvt_pk_f16_f32 v70, v98, v99
	v_cvt_pk_f16_f32 v71, v101, v71
	v_cvt_pk_f16_f32 v64, v103, v104
	v_cvt_pk_f16_f32 v65, v105, v106
	v_cvt_pk_f16_f32 v66, v107, v108
	v_cvt_pk_f16_f32 v67, v109, v110
	s_nop 1
	v_permlane32_swap_b32_e32 v80, v81
	v_permlane32_swap_b32_e32 v76, v78
	v_permlane32_swap_b32_e32 v77, v79
	v_permlane32_swap_b32_e32 v72, v74
	v_permlane32_swap_b32_e32 v73, v75
	v_permlane32_swap_b32_e32 v68, v70
	v_permlane32_swap_b32_e32 v69, v71
	v_permlane32_swap_b32_e32 v64, v66
	v_permlane32_swap_b32_e32 v65, v67
	v_cmp_gt_f32_e32 vcc, 1.0, v102
	s_cbranch_vccz .LBB1_11
	v_pk_mul_f32 v[62:63], v[102:103], v[62:63] op_sel_hi:[0,1]
	v_pk_mul_f32 v[60:61], v[102:103], v[60:61] op_sel_hi:[0,1]
	v_pk_mul_f32 v[58:59], v[102:103], v[58:59] op_sel_hi:[0,1]
	v_pk_mul_f32 v[56:57], v[102:103], v[56:57] op_sel_hi:[0,1]
	v_pk_mul_f32 v[54:55], v[102:103], v[54:55] op_sel_hi:[0,1]
	v_pk_mul_f32 v[52:53], v[102:103], v[52:53] op_sel_hi:[0,1]
	v_pk_mul_f32 v[50:51], v[102:103], v[50:51] op_sel_hi:[0,1]
	v_pk_mul_f32 v[48:49], v[102:103], v[48:49] op_sel_hi:[0,1]
	v_pk_mul_f32 v[46:47], v[102:103], v[46:47] op_sel_hi:[0,1]
	v_pk_mul_f32 v[44:45], v[102:103], v[44:45] op_sel_hi:[0,1]
	v_pk_mul_f32 v[42:43], v[102:103], v[42:43] op_sel_hi:[0,1]
	v_pk_mul_f32 v[40:41], v[102:103], v[40:41] op_sel_hi:[0,1]
	v_pk_mul_f32 v[38:39], v[102:103], v[38:39] op_sel_hi:[0,1]
	v_pk_mul_f32 v[36:37], v[102:103], v[36:37] op_sel_hi:[0,1]
	v_pk_mul_f32 v[34:35], v[102:103], v[34:35] op_sel_hi:[0,1]
	v_pk_mul_f32 v[32:33], v[102:103], v[32:33] op_sel_hi:[0,1]
	v_pk_mul_f32 v[30:31], v[102:103], v[30:31] op_sel_hi:[0,1]
	v_pk_mul_f32 v[28:29], v[102:103], v[28:29] op_sel_hi:[0,1]
	v_pk_mul_f32 v[26:27], v[102:103], v[26:27] op_sel_hi:[0,1]
	v_pk_mul_f32 v[24:25], v[102:103], v[24:25] op_sel_hi:[0,1]
	v_pk_mul_f32 v[22:23], v[102:103], v[22:23] op_sel_hi:[0,1]
	v_pk_mul_f32 v[20:21], v[102:103], v[20:21] op_sel_hi:[0,1]
	v_pk_mul_f32 v[18:19], v[102:103], v[18:19] op_sel_hi:[0,1]
	v_pk_mul_f32 v[16:17], v[102:103], v[16:17] op_sel_hi:[0,1]
	v_pk_mul_f32 v[14:15], v[102:103], v[14:15] op_sel_hi:[0,1]
	v_pk_mul_f32 v[12:13], v[102:103], v[12:13] op_sel_hi:[0,1]
	v_pk_mul_f32 v[10:11], v[102:103], v[10:11] op_sel_hi:[0,1]
	v_pk_mul_f32 v[8:9], v[102:103], v[8:9] op_sel_hi:[0,1]
	v_pk_mul_f32 v[6:7], v[102:103], v[6:7] op_sel_hi:[0,1]
	v_pk_mul_f32 v[4:5], v[102:103], v[4:5] op_sel_hi:[0,1]
	v_pk_mul_f32 v[2:3], v[102:103], v[2:3] op_sel_hi:[0,1]
	v_pk_mul_f32 v[0:1], v[102:103], v[0:1] op_sel_hi:[0,1]
.LBB1_11:
	v_add_f32_e32 v82, v112, v113
	v_add_f32_e32 v101, v80, v81
	v_fmac_f32_e32 v82, v165, v166
	ds_read_b64_tr_b16 v[84:85], v163 offset:0
	ds_read_b64_tr_b16 v[86:87], v167 offset:0
	ds_read_b64_tr_b16 v[88:89], v163 offset:0x1000
	ds_read_b64_tr_b16 v[90:91], v167 offset:0x1000
	ds_read_b64_tr_b16 v[92:93], v163 offset:0x2000
	ds_read_b64_tr_b16 v[94:95], v167 offset:0x2000
	ds_read_b64_tr_b16 v[96:97], v163 offset:0x3000
	ds_read_b64_tr_b16 v[98:99], v167 offset:0x3000
	ds_read_b64_tr_b16 v[104:105], v163 offset:0x200
	ds_read_b64_tr_b16 v[106:107], v167 offset:0x200
	ds_read_b64_tr_b16 v[108:109], v163 offset:0x1200
	ds_read_b64_tr_b16 v[110:111], v167 offset:0x1200
	ds_read_b64_tr_b16 v[112:113], v163 offset:0x2200
	ds_read_b64_tr_b16 v[114:115], v167 offset:0x2200
	ds_read_b64_tr_b16 v[116:117], v163 offset:0x3200
	ds_read_b64_tr_b16 v[118:119], v167 offset:0x3200
	s_nop 0
	s_waitcnt lgkmcnt(14)
	v_mfma_f32_32x32x16_f16 v[48:63], v[84:87], v[76:79], v[48:63]
	ds_read_b64_tr_b16 v[84:85], v163 offset:0x400
	ds_read_b64_tr_b16 v[86:87], v167 offset:0x400
	s_waitcnt lgkmcnt(8)
	v_mfma_f32_32x32x16_f16 v[32:47], v[104:107], v[76:79], v[32:47]
	v_mfma_f32_32x32x16_f16 v[48:63], v[88:91], v[72:75], v[48:63]
	ds_read_b64_tr_b16 v[88:89], v163 offset:0x1400
	ds_read_b64_tr_b16 v[90:91], v167 offset:0x1400
	s_waitcnt lgkmcnt(8)
	v_mfma_f32_32x32x16_f16 v[32:47], v[108:111], v[72:75], v[32:47]
	v_mfma_f32_32x32x16_f16 v[48:63], v[92:95], v[68:71], v[48:63]
	ds_read_b64_tr_b16 v[92:93], v163 offset:0x2400
	ds_read_b64_tr_b16 v[94:95], v167 offset:0x2400
	ds_read_b64_tr_b16 v[104:105], v163 offset:0x3400
	ds_read_b64_tr_b16 v[106:107], v167 offset:0x3400
	ds_read_b64_tr_b16 v[108:109], v163 offset:0x600
	ds_read_b64_tr_b16 v[110:111], v167 offset:0x600
	s_waitcnt lgkmcnt(12)
	v_mfma_f32_32x32x16_f16 v[32:47], v[112:115], v[68:71], v[32:47]
	v_mfma_f32_32x32x16_f16 v[48:63], v[96:99], v[64:67], v[48:63]
	ds_read_b64_tr_b16 v[96:97], v163 offset:0x1600
	ds_read_b64_tr_b16 v[98:99], v167 offset:0x1600
	ds_read_b64_tr_b16 v[112:113], v163 offset:0x2600
	ds_read_b64_tr_b16 v[114:115], v167 offset:0x2600
	ds_read_b64_tr_b16 v[120:121], v163 offset:0x3600
	ds_read_b64_tr_b16 v[122:123], v167 offset:0x3600
	s_waitcnt lgkmcnt(15)
	v_mfma_f32_32x32x16_f16 v[32:47], v[116:119], v[64:67], v[32:47]
	s_waitcnt lgkmcnt(14)
	v_mfma_f32_32x32x16_f16 v[16:31], v[84:87], v[76:79], v[16:31]
	s_lshl_b64 s[2:3], s[28:29], 14
	v_mov_b32_e32 v163, 0
	s_add_u32 s0, s0, s2
	v_cmp_lt_u32_e32 vcc, 31, v161
	s_addc_u32 s1, s1, s3
	s_waitcnt lgkmcnt(6)
	v_mfma_f32_32x32x16_f16 v[0:15], v[108:111], v[76:79], v[0:15]
	v_mfma_f32_32x32x16_f16 v[16:31], v[88:91], v[72:75], v[16:31]
	s_waitcnt lgkmcnt(4)
	v_mfma_f32_32x32x16_f16 v[0:15], v[96:99], v[72:75], v[0:15]
	v_mfma_f32_32x32x16_f16 v[16:31], v[92:95], v[68:71], v[16:31]
	s_waitcnt lgkmcnt(2)
	v_mfma_f32_32x32x16_f16 v[0:15], v[112:115], v[68:71], v[0:15]
	v_mov_b32_e32 v69, v163
	v_mfma_f32_32x32x16_f16 v[16:31], v[104:107], v[64:67], v[16:31]
	s_waitcnt lgkmcnt(0)
	v_mfma_f32_32x32x16_f16 v[0:15], v[120:123], v[64:67], v[0:15]
	s_and_saveexec_b64 s[2:3], vcc
	s_xor_b64 s[2:3], exec, s[2:3]
	s_or_saveexec_b64 s[2:3], s[2:3]
	v_fmac_f32_e32 v101, v82, v102
	v_lshl_add_u64 v[64:65], s[0:1], 0, v[162:163]
	s_xor_b64 exec, exec, s[2:3]
	s_cbranch_execz .LBB1_13
	v_lshl_add_u64 v[66:67], v[64:65], 3, s[26:27]
	v_lshlrev_b32_e32 v70, 3, v160
	v_mov_b32_e32 v71, 0
	v_lshl_add_u64 v[66:67], v[66:67], 0, v[70:71]
	global_store_dwordx2 v[66:67], v[100:101], off

	.amdhsa_kernel _Z11attn_kernelPKDF16_S0_PDF16_P15HIP_vector_typeIfLj2EE
		.amdhsa_group_segment_fixed_size 0
		.amdhsa_private_segment_fixed_size 0
		.amdhsa_kernarg_size 32
		.amdhsa_user_sgpr_count 2
		.amdhsa_user_sgpr_dispatch_ptr 0
		.amdhsa_user_sgpr_queue_ptr 0
		.amdhsa_user_sgpr_kernarg_segment_ptr 1
		.amdhsa_user_sgpr_dispatch_id 0
		.amdhsa_user_sgpr_kernarg_preload_length 0
		.amdhsa_user_sgpr_kernarg_preload_offset 0
		.amdhsa_user_sgpr_private_segment_size 0
		.amdhsa_uses_dynamic_stack 0
		.amdhsa_enable_private_segment 0
		.amdhsa_system_sgpr_workgroup_id_x 1
		.amdhsa_system_sgpr_workgroup_id_y 1
		.amdhsa_system_sgpr_workgroup_id_z 1
		.amdhsa_system_sgpr_workgroup_info 0
		.amdhsa_system_vgpr_workitem_id 0
		.amdhsa_next_free_vgpr 244
		.amdhsa_next_free_sgpr 40
		.amdhsa_accum_offset 244
		.amdhsa_reserve_vcc 1
		.amdhsa_float_round_mode_32 0
		.amdhsa_float_round_mode_16_64 0
		.amdhsa_float_denorm_mode_32 3
		.amdhsa_float_denorm_mode_16_64 3
		.amdhsa_dx10_clamp 1
		.amdhsa_ieee_mode 1
		.amdhsa_fp16_overflow 0
		.amdhsa_tg_split 0
		.amdhsa_exception_fp_ieee_invalid_op 0
		.amdhsa_exception_fp_denorm_src 0
		.amdhsa_exception_fp_ieee_div_zero 0
		.amdhsa_exception_fp_ieee_overflow 0
		.amdhsa_exception_fp_ieee_underflow 0
		.amdhsa_exception_fp_ieee_inexact 0
		.amdhsa_exception_int_div_zero 0
	.end_amdhsa_kernel

_Z19combine_proj_kernelPKDF16_PK15HIP_vector_typeIfLj2EES0_PKfPf:
	s_load_dwordx8 s[4:11], s[0:1], 0x0
	s_load_dwordx2 s[12:13], s[0:1], 0x20
	v_and_b32_e32 v1, 15, v0
	v_lshrrev_b32_e32 v2, 4, v0
	s_lshl_b32 s3, s2, 9
	s_lshl_b32 s14, s2, 14
	s_lshl_b32 s15, s2, 15
	v_lshl_add_u32 v3, v2, 3, s3
	v_lshlrev_b32_e32 v4, 8, v2
	v_lshl_add_u32 v4, v1, 4, v4
	v_add_u32_e32 v4, s14, v4
	v_add_u32_e32 v5, 0x1000, v4
	v_add_u32_e32 v6, 0x2000, v4
	v_add_u32_e32 v7, 0x3000, v4
	v_lshrrev_b32_e32 v8, 6, v0
	v_and_b32_e32 v9, 63, v0
	v_and_b32_e32 v10, 31, v0
	v_bfe_u32 v11, v0, 5, 1
	v_and_b32_e32 v18, 1, v8
	v_lshrrev_b32_e32 v19, 1, v8
	v_lshlrev_b32_e32 v12, 14, v19
	v_lshl_add_u32 v12, v10, 8, v12
	v_lshl_add_u32 v12, v11, 4, v12
	v_add_u32_e32 v13, 0x2000, v12
	v_lshlrev_b32_e32 v14, 8, v19
	v_lshl_add_u32 v14, v10, 2, v14
	s_waitcnt lgkmcnt(0)
	s_add_u32 s16, s6, 0x20000
	s_addc_u32 s17, s7, 0
	s_add_u32 s18, s6, 0x40000
	s_addc_u32 s19, s7, 0
	s_add_u32 s20, s6, 0x60000
	s_addc_u32 s21, s7, 0
	s_add_u32 s22, s4, 0x400000
	s_addc_u32 s23, s5, 0
	s_add_u32 s24, s4, 0x800000
	s_addc_u32 s25, s5, 0
	s_add_u32 s26, s4, 0xc00000
	s_addc_u32 s27, s5, 0
	global_load_dwordx2 v[20:21], v3, s[6:7] offset:0
	global_load_dwordx2 v[22:23], v3, s[16:17] offset:0
	global_load_dwordx2 v[24:25], v3, s[18:19] offset:0
	global_load_dwordx2 v[26:27], v3, s[20:21] offset:0
	global_load_dwordx2 v[28:29], v3, s[6:7] offset:128
	global_load_dwordx2 v[30:31], v3, s[16:17] offset:128
	global_load_dwordx2 v[32:33], v3, s[18:19] offset:128
	global_load_dwordx2 v[34:35], v3, s[20:21] offset:128
	global_load_dwordx2 v[36:37], v3, s[6:7] offset:256
	global_load_dwordx2 v[38:39], v3, s[16:17] offset:256
	global_load_dwordx2 v[40:41], v3, s[18:19] offset:256
	global_load_dwordx2 v[42:43], v3, s[20:21] offset:256
	global_load_dwordx2 v[44:45], v3, s[6:7] offset:384
	global_load_dwordx2 v[46:47], v3, s[16:17] offset:384
	global_load_dwordx2 v[48:49], v3, s[18:19] offset:384
	global_load_dwordx2 v[50:51], v3, s[20:21] offset:384
	global_load_dwordx4 v[52:55], v4, s[4:5]
	global_load_dwordx4 v[56:59], v4, s[22:23]
	global_load_dwordx4 v[60:63], v4, s[24:25]
	global_load_dwordx4 v[64:67], v4, s[26:27]
	global_load_dwordx4 v[68:71], v5, s[4:5]
	global_load_dwordx4 v[72:75], v5, s[22:23]
	global_load_dwordx4 v[76:79], v5, s[24:25]
	global_load_dwordx4 v[80:83], v5, s[26:27]
	global_load_dwordx4 v[84:87], v6, s[4:5]
	global_load_dwordx4 v[88:91], v6, s[22:23]
	global_load_dwordx4 v[92:95], v6, s[24:25]
	global_load_dwordx4 v[96:99], v6, s[26:27]
	global_load_dwordx4 v[100:103], v7, s[4:5]
	global_load_dwordx4 v[104:107], v7, s[22:23]
	global_load_dwordx4 v[108:111], v7, s[24:25]
	global_load_dwordx4 v[112:115], v7, s[26:27]
	global_load_dwordx4 v[116:119], v12, s[8:9] offset:0
	global_load_dwordx4 v[120:123], v12, s[8:9] offset:32
	global_load_dwordx4 v[124:127], v12, s[8:9] offset:64
	global_load_dwordx4 v[128:131], v12, s[8:9] offset:96
	global_load_dwordx4 v[132:135], v12, s[8:9] offset:128
	global_load_dwordx4 v[136:139], v12, s[8:9] offset:160
	global_load_dwordx4 v[140:143], v12, s[8:9] offset:192
	global_load_dwordx4 v[144:147], v12, s[8:9] offset:224
	global_load_dwordx4 v[148:151], v13, s[8:9] offset:0
	global_load_dwordx4 v[152:155], v13, s[8:9] offset:32
	global_load_dwordx4 v[156:159], v13, s[8:9] offset:64
	global_load_dwordx4 v[160:163], v13, s[8:9] offset:96
	global_load_dwordx4 v[164:167], v13, s[8:9] offset:128
	global_load_dwordx4 v[168:171], v13, s[8:9] offset:160
	global_load_dwordx4 v[172:175], v13, s[8:9] offset:192
	global_load_dwordx4 v[176:179], v13, s[8:9] offset:224
	global_load_dword v180, v14, s[10:11]
	global_load_dword v181, v14, s[10:11] offset:128
	v_mul_u32_u24_e32 v15, 0x110, v2
	v_lshl_add_u32 v15, v1, 4, v15
	v_lshl_add_u32 v16, v18, 5, v10
	v_mul_u32_u24_e32 v16, 0x110, v16
	v_lshl_add_u32 v16, v11, 4, v16
	v_lshlrev_b32_e32 v17, 14, v18
	v_lshl_add_u32 v17, v11, 11, v17
	v_add3_u32 v17, v17, v14, s15
	s_mov_b32 s28, s12
	s_and_b32 s29, s13, 0xffff
	s_mov_b32 s30, 0x800000
	s_mov_b32 s31, 0x20000
	s_movk_i32 s33, 0x1000
	s_movk_i32 s34, 0x2000
	s_movk_i32 s35, 0x3000
	s_waitcnt vmcnt(30)
	v_max3_f32 v182, v20, v22, v24
	v_max_f32_e32 v182, v182, v26
	v_sub_f32_e32 v183, v20, v182
	v_sub_f32_e32 v184, v22, v182
	v_sub_f32_e32 v185, v24, v182
	v_sub_f32_e32 v186, v26, v182
	v_exp_f32_e32 v183, v183
	v_exp_f32_e32 v184, v184
	v_exp_f32_e32 v185, v185
	v_exp_f32_e32 v186, v186
	s_nop 0
	v_mul_f32_e32 v183, v183, v21
	v_mul_f32_e32 v184, v184, v23
	v_mul_f32_e32 v185, v185, v25
	v_mul_f32_e32 v186, v186, v27
	v_add_f32_e32 v187, v183, v184
	v_add_f32_e32 v187, v187, v185
	v_add_f32_e32 v187, v187, v186
	v_rcp_f32_e32 v187, v187
	s_nop 0
	v_mul_f32_e32 v188, v183, v187
	v_mul_f32_e32 v189, v184, v187
	v_mul_f32_e32 v190, v185, v187
	v_mul_f32_e32 v191, v186, v187
	v_fma_mix_f32 v192, v188, v52, 0 op_sel_hi:[0,1,0]
	v_fma_mix_f32 v193, v188, v52, 0 op_sel:[0,1,0] op_sel_hi:[0,1,0]
	v_fma_mix_f32 v194, v188, v53, 0 op_sel_hi:[0,1,0]
	v_fma_mix_f32 v195, v188, v53, 0 op_sel:[0,1,0] op_sel_hi:[0,1,0]
	v_fma_mix_f32 v196, v188, v54, 0 op_sel_hi:[0,1,0]
	v_fma_mix_f32 v197, v188, v54, 0 op_sel:[0,1,0] op_sel_hi:[0,1,0]
	v_fma_mix_f32 v198, v188, v55, 0 op_sel_hi:[0,1,0]
	v_fma_mix_f32 v199, v188, v55, 0 op_sel:[0,1,0] op_sel_hi:[0,1,0]
	v_fma_mix_f32 v192, v189, v56, v192 op_sel_hi:[0,1,0]
	v_fma_mix_f32 v193, v189, v56, v193 op_sel:[0,1,0] op_sel_hi:[0,1,0]
	v_fma_mix_f32 v194, v189, v57, v194 op_sel_hi:[0,1,0]
	v_fma_mix_f32 v195, v189, v57, v195 op_sel:[0,1,0] op_sel_hi:[0,1,0]
	v_fma_mix_f32 v196, v189, v58, v196 op_sel_hi:[0,1,0]
	v_fma_mix_f32 v197, v189, v58, v197 op_sel:[0,1,0] op_sel_hi:[0,1,0]
	v_fma_mix_f32 v198, v189, v59, v198 op_sel_hi:[0,1,0]
	v_fma_mix_f32 v199, v189, v59, v199 op_sel:[0,1,0] op_sel_hi:[0,1,0]
	v_fma_mix_f32 v192, v190, v60, v192 op_sel_hi:[0,1,0]
	v_fma_mix_f32 v193, v190, v60, v193 op_sel:[0,1,0] op_sel_hi:[0,1,0]
	v_fma_mix_f32 v194, v190, v61, v194 op_sel_hi:[0,1,0]
	v_fma_mix_f32 v195, v190, v61, v195 op_sel:[0,1,0] op_sel_hi:[0,1,0]
	v_fma_mix_f32 v196, v190, v62, v196 op_sel_hi:[0,1,0]
	v_fma_mix_f32 v197, v190, v62, v197 op_sel:[0,1,0] op_sel_hi:[0,1,0]
	v_fma_mix_f32 v198, v190, v63, v198 op_sel_hi:[0,1,0]
	v_fma_mix_f32 v199, v190, v63, v199 op_sel:[0,1,0] op_sel_hi:[0,1,0]
	v_fma_mix_f32 v192, v191, v64, v192 op_sel_hi:[0,1,0]
	v_fma_mix_f32 v193, v191, v64, v193 op_sel:[0,1,0] op_sel_hi:[0,1,0]
	v_fma_mix_f32 v194, v191, v65, v194 op_sel_hi:[0,1,0]
	v_fma_mix_f32 v195, v191, v65, v195 op_sel:[0,1,0] op_sel_hi:[0,1,0]
	v_fma_mix_f32 v196, v191, v66, v196 op_sel_hi:[0,1,0]
	v_fma_mix_f32 v197, v191, v66, v197 op_sel:[0,1,0] op_sel_hi:[0,1,0]
	v_fma_mix_f32 v198, v191, v67, v198 op_sel_hi:[0,1,0]
	v_fma_mix_f32 v199, v191, v67, v199 op_sel:[0,1,0] op_sel_hi:[0,1,0]
	v_cvt_pk_f16_f32 v200, v192, v193
	v_cvt_pk_f16_f32 v201, v194, v195
	v_cvt_pk_f16_f32 v202, v196, v197
	v_cvt_pk_f16_f32 v203, v198, v199
	ds_write_b128 v15, v[200:203] offset:0
	s_waitcnt vmcnt(26)
	v_max3_f32 v182, v28, v30, v32
	v_max_f32_e32 v182, v182, v34
	v_sub_f32_e32 v183, v28, v182
	v_sub_f32_e32 v184, v30, v182
	v_sub_f32_e32 v185, v32, v182
	v_sub_f32_e32 v186, v34, v182
	v_exp_f32_e32 v183, v183
	v_exp_f32_e32 v184, v184
	v_exp_f32_e32 v185, v185
	v_exp_f32_e32 v186, v186
	s_nop 0
	v_mul_f32_e32 v183, v183, v29
	v_mul_f32_e32 v184, v184, v31
	v_mul_f32_e32 v185, v185, v33
	v_mul_f32_e32 v186, v186, v35
	v_add_f32_e32 v187, v183, v184
	v_add_f32_e32 v187, v187, v185
	v_add_f32_e32 v187, v187, v186
	v_rcp_f32_e32 v187, v187
	s_nop 0
	v_mul_f32_e32 v188, v183, v187
	v_mul_f32_e32 v189, v184, v187
	v_mul_f32_e32 v190, v185, v187
	v_mul_f32_e32 v191, v186, v187
	v_fma_mix_f32 v192, v188, v68, 0 op_sel_hi:[0,1,0]
	v_fma_mix_f32 v193, v188, v68, 0 op_sel:[0,1,0] op_sel_hi:[0,1,0]
	v_fma_mix_f32 v194, v188, v69, 0 op_sel_hi:[0,1,0]
	v_fma_mix_f32 v195, v188, v69, 0 op_sel:[0,1,0] op_sel_hi:[0,1,0]
	v_fma_mix_f32 v196, v188, v70, 0 op_sel_hi:[0,1,0]
	v_fma_mix_f32 v197, v188, v70, 0 op_sel:[0,1,0] op_sel_hi:[0,1,0]
	v_fma_mix_f32 v198, v188, v71, 0 op_sel_hi:[0,1,0]
	v_fma_mix_f32 v199, v188, v71, 0 op_sel:[0,1,0] op_sel_hi:[0,1,0]
	v_fma_mix_f32 v192, v189, v72, v192 op_sel_hi:[0,1,0]
	v_fma_mix_f32 v193, v189, v72, v193 op_sel:[0,1,0] op_sel_hi:[0,1,0]
	v_fma_mix_f32 v194, v189, v73, v194 op_sel_hi:[0,1,0]
	v_fma_mix_f32 v195, v189, v73, v195 op_sel:[0,1,0] op_sel_hi:[0,1,0]
	v_fma_mix_f32 v196, v189, v74, v196 op_sel_hi:[0,1,0]
	v_fma_mix_f32 v197, v189, v74, v197 op_sel:[0,1,0] op_sel_hi:[0,1,0]
	v_fma_mix_f32 v198, v189, v75, v198 op_sel_hi:[0,1,0]
	v_fma_mix_f32 v199, v189, v75, v199 op_sel:[0,1,0] op_sel_hi:[0,1,0]
	v_fma_mix_f32 v192, v190, v76, v192 op_sel_hi:[0,1,0]
	v_fma_mix_f32 v193, v190, v76, v193 op_sel:[0,1,0] op_sel_hi:[0,1,0]
	v_fma_mix_f32 v194, v190, v77, v194 op_sel_hi:[0,1,0]
	v_fma_mix_f32 v195, v190, v77, v195 op_sel:[0,1,0] op_sel_hi:[0,1,0]
	v_fma_mix_f32 v196, v190, v78, v196 op_sel_hi:[0,1,0]
	v_fma_mix_f32 v197, v190, v78, v197 op_sel:[0,1,0] op_sel_hi:[0,1,0]
	v_fma_mix_f32 v198, v190, v79, v198 op_sel_hi:[0,1,0]
	v_fma_mix_f32 v199, v190, v79, v199 op_sel:[0,1,0] op_sel_hi:[0,1,0]
	v_fma_mix_f32 v192, v191, v80, v192 op_sel_hi:[0,1,0]
	v_fma_mix_f32 v193, v191, v80, v193 op_sel:[0,1,0] op_sel_hi:[0,1,0]
	v_fma_mix_f32 v194, v191, v81, v194 op_sel_hi:[0,1,0]
	v_fma_mix_f32 v195, v191, v81, v195 op_sel:[0,1,0] op_sel_hi:[0,1,0]
	v_fma_mix_f32 v196, v191, v82, v196 op_sel_hi:[0,1,0]
	v_fma_mix_f32 v197, v191, v82, v197 op_sel:[0,1,0] op_sel_hi:[0,1,0]
	v_fma_mix_f32 v198, v191, v83, v198 op_sel_hi:[0,1,0]
	v_fma_mix_f32 v199, v191, v83, v199 op_sel:[0,1,0] op_sel_hi:[0,1,0]
	v_cvt_pk_f16_f32 v200, v192, v193
	v_cvt_pk_f16_f32 v201, v194, v195
	v_cvt_pk_f16_f32 v202, v196, v197
	v_cvt_pk_f16_f32 v203, v198, v199
	ds_write_b128 v15, v[200:203] offset:4352
	s_waitcnt vmcnt(22)
	v_max3_f32 v182, v36, v38, v40
	v_max_f32_e32 v182, v182, v42
	v_sub_f32_e32 v183, v36, v182
	v_sub_f32_e32 v184, v38, v182
	v_sub_f32_e32 v185, v40, v182
	v_sub_f32_e32 v186, v42, v182
	v_exp_f32_e32 v183, v183
	v_exp_f32_e32 v184, v184
	v_exp_f32_e32 v185, v185
	v_exp_f32_e32 v186, v186
	s_nop 0
	v_mul_f32_e32 v183, v183, v37
	v_mul_f32_e32 v184, v184, v39
	v_mul_f32_e32 v185, v185, v41
	v_mul_f32_e32 v186, v186, v43
	v_add_f32_e32 v187, v183, v184
	v_add_f32_e32 v187, v187, v185
	v_add_f32_e32 v187, v187, v186
	v_rcp_f32_e32 v187, v187
	s_nop 0
	v_mul_f32_e32 v188, v183, v187
	v_mul_f32_e32 v189, v184, v187
	v_mul_f32_e32 v190, v185, v187
	v_mul_f32_e32 v191, v186, v187
	v_fma_mix_f32 v192, v188, v84, 0 op_sel_hi:[0,1,0]
	v_fma_mix_f32 v193, v188, v84, 0 op_sel:[0,1,0] op_sel_hi:[0,1,0]
	v_fma_mix_f32 v194, v188, v85, 0 op_sel_hi:[0,1,0]
	v_fma_mix_f32 v195, v188, v85, 0 op_sel:[0,1,0] op_sel_hi:[0,1,0]
	v_fma_mix_f32 v196, v188, v86, 0 op_sel_hi:[0,1,0]
	v_fma_mix_f32 v197, v188, v86, 0 op_sel:[0,1,0] op_sel_hi:[0,1,0]
	v_fma_mix_f32 v198, v188, v87, 0 op_sel_hi:[0,1,0]
	v_fma_mix_f32 v199, v188, v87, 0 op_sel:[0,1,0] op_sel_hi:[0,1,0]
	v_fma_mix_f32 v192, v189, v88, v192 op_sel_hi:[0,1,0]
	v_fma_mix_f32 v193, v189, v88, v193 op_sel:[0,1,0] op_sel_hi:[0,1,0]
	v_fma_mix_f32 v194, v189, v89, v194 op_sel_hi:[0,1,0]
	v_fma_mix_f32 v195, v189, v89, v195 op_sel:[0,1,0] op_sel_hi:[0,1,0]
	v_fma_mix_f32 v196, v189, v90, v196 op_sel_hi:[0,1,0]
	v_fma_mix_f32 v197, v189, v90, v197 op_sel:[0,1,0] op_sel_hi:[0,1,0]
	v_fma_mix_f32 v198, v189, v91, v198 op_sel_hi:[0,1,0]
	v_fma_mix_f32 v199, v189, v91, v199 op_sel:[0,1,0] op_sel_hi:[0,1,0]
	v_fma_mix_f32 v192, v190, v92, v192 op_sel_hi:[0,1,0]
	v_fma_mix_f32 v193, v190, v92, v193 op_sel:[0,1,0] op_sel_hi:[0,1,0]
	v_fma_mix_f32 v194, v190, v93, v194 op_sel_hi:[0,1,0]
	v_fma_mix_f32 v195, v190, v93, v195 op_sel:[0,1,0] op_sel_hi:[0,1,0]
	v_fma_mix_f32 v196, v190, v94, v196 op_sel_hi:[0,1,0]
	v_fma_mix_f32 v197, v190, v94, v197 op_sel:[0,1,0] op_sel_hi:[0,1,0]
	v_fma_mix_f32 v198, v190, v95, v198 op_sel_hi:[0,1,0]
	v_fma_mix_f32 v199, v190, v95, v199 op_sel:[0,1,0] op_sel_hi:[0,1,0]
	v_fma_mix_f32 v192, v191, v96, v192 op_sel_hi:[0,1,0]
	v_fma_mix_f32 v193, v191, v96, v193 op_sel:[0,1,0] op_sel_hi:[0,1,0]
	v_fma_mix_f32 v194, v191, v97, v194 op_sel_hi:[0,1,0]
	v_fma_mix_f32 v195, v191, v97, v195 op_sel:[0,1,0] op_sel_hi:[0,1,0]
	v_fma_mix_f32 v196, v191, v98, v196 op_sel_hi:[0,1,0]
	v_fma_mix_f32 v197, v191, v98, v197 op_sel:[0,1,0] op_sel_hi:[0,1,0]
	v_fma_mix_f32 v198, v191, v99, v198 op_sel_hi:[0,1,0]
	v_fma_mix_f32 v199, v191, v99, v199 op_sel:[0,1,0] op_sel_hi:[0,1,0]
	v_cvt_pk_f16_f32 v200, v192, v193
	v_cvt_pk_f16_f32 v201, v194, v195
	v_cvt_pk_f16_f32 v202, v196, v197
	v_cvt_pk_f16_f32 v203, v198, v199
	ds_write_b128 v15, v[200:203] offset:8704
	s_waitcnt vmcnt(18)
	v_max3_f32 v182, v44, v46, v48
	v_max_f32_e32 v182, v182, v50
	v_sub_f32_e32 v183, v44, v182
	v_sub_f32_e32 v184, v46, v182
	v_sub_f32_e32 v185, v48, v182
	v_sub_f32_e32 v186, v50, v182
	v_exp_f32_e32 v183, v183
	v_exp_f32_e32 v184, v184
	v_exp_f32_e32 v185, v185
	v_exp_f32_e32 v186, v186
	s_nop 0
	v_mul_f32_e32 v183, v183, v45
	v_mul_f32_e32 v184, v184, v47
	v_mul_f32_e32 v185, v185, v49
	v_mul_f32_e32 v186, v186, v51
	v_add_f32_e32 v187, v183, v184
	v_add_f32_e32 v187, v187, v185
	v_add_f32_e32 v187, v187, v186
	v_rcp_f32_e32 v187, v187
	s_nop 0
	v_mul_f32_e32 v188, v183, v187
	v_mul_f32_e32 v189, v184, v187
	v_mul_f32_e32 v190, v185, v187
	v_mul_f32_e32 v191, v186, v187
	v_fma_mix_f32 v192, v188, v100, 0 op_sel_hi:[0,1,0]
	v_fma_mix_f32 v193, v188, v100, 0 op_sel:[0,1,0] op_sel_hi:[0,1,0]
	v_fma_mix_f32 v194, v188, v101, 0 op_sel_hi:[0,1,0]
	v_fma_mix_f32 v195, v188, v101, 0 op_sel:[0,1,0] op_sel_hi:[0,1,0]
	v_fma_mix_f32 v196, v188, v102, 0 op_sel_hi:[0,1,0]
	v_fma_mix_f32 v197, v188, v102, 0 op_sel:[0,1,0] op_sel_hi:[0,1,0]
	v_fma_mix_f32 v198, v188, v103, 0 op_sel_hi:[0,1,0]
	v_fma_mix_f32 v199, v188, v103, 0 op_sel:[0,1,0] op_sel_hi:[0,1,0]
	v_fma_mix_f32 v192, v189, v104, v192 op_sel_hi:[0,1,0]
	v_fma_mix_f32 v193, v189, v104, v193 op_sel:[0,1,0] op_sel_hi:[0,1,0]
	v_fma_mix_f32 v194, v189, v105, v194 op_sel_hi:[0,1,0]
	v_fma_mix_f32 v195, v189, v105, v195 op_sel:[0,1,0] op_sel_hi:[0,1,0]
	v_fma_mix_f32 v196, v189, v106, v196 op_sel_hi:[0,1,0]
	v_fma_mix_f32 v197, v189, v106, v197 op_sel:[0,1,0] op_sel_hi:[0,1,0]
	v_fma_mix_f32 v198, v189, v107, v198 op_sel_hi:[0,1,0]
	v_fma_mix_f32 v199, v189, v107, v199 op_sel:[0,1,0] op_sel_hi:[0,1,0]
	v_fma_mix_f32 v192, v190, v108, v192 op_sel_hi:[0,1,0]
	v_fma_mix_f32 v193, v190, v108, v193 op_sel:[0,1,0] op_sel_hi:[0,1,0]
	v_fma_mix_f32 v194, v190, v109, v194 op_sel_hi:[0,1,0]
	v_fma_mix_f32 v195, v190, v109, v195 op_sel:[0,1,0] op_sel_hi:[0,1,0]
	v_fma_mix_f32 v196, v190, v110, v196 op_sel_hi:[0,1,0]
	v_fma_mix_f32 v197, v190, v110, v197 op_sel:[0,1,0] op_sel_hi:[0,1,0]
	v_fma_mix_f32 v198, v190, v111, v198 op_sel_hi:[0,1,0]
	v_fma_mix_f32 v199, v190, v111, v199 op_sel:[0,1,0] op_sel_hi:[0,1,0]
	v_fma_mix_f32 v192, v191, v112, v192 op_sel_hi:[0,1,0]
	v_fma_mix_f32 v193, v191, v112, v193 op_sel:[0,1,0] op_sel_hi:[0,1,0]
	v_fma_mix_f32 v194, v191, v113, v194 op_sel_hi:[0,1,0]
	v_fma_mix_f32 v195, v191, v113, v195 op_sel:[0,1,0] op_sel_hi:[0,1,0]
	v_fma_mix_f32 v196, v191, v114, v196 op_sel_hi:[0,1,0]
	v_fma_mix_f32 v197, v191, v114, v197 op_sel:[0,1,0] op_sel_hi:[0,1,0]
	v_fma_mix_f32 v198, v191, v115, v198 op_sel_hi:[0,1,0]
	v_fma_mix_f32 v199, v191, v115, v199 op_sel:[0,1,0] op_sel_hi:[0,1,0]
	v_cvt_pk_f16_f32 v200, v192, v193
	v_cvt_pk_f16_f32 v201, v194, v195
	v_cvt_pk_f16_f32 v202, v196, v197
	v_cvt_pk_f16_f32 v203, v198, v199
	ds_write_b128 v15, v[200:203] offset:13056
	s_waitcnt lgkmcnt(0)
	s_barrier
	ds_read_b128 v[52:55], v16 offset:0
	ds_read_b128 v[56:59], v16 offset:32
	ds_read_b128 v[60:63], v16 offset:64
	ds_read_b128 v[64:67], v16 offset:96
	ds_read_b128 v[68:71], v16 offset:128
	ds_read_b128 v[72:75], v16 offset:160
	ds_read_b128 v[76:79], v16 offset:192
	ds_read_b128 v[80:83], v16 offset:224
	s_waitcnt vmcnt(0)
	s_waitcnt lgkmcnt(7)
	v_mfma_f32_32x32x16_f16 v[84:99], v[52:55], v[116:119], 0
	v_mfma_f32_32x32x16_f16 v[100:115], v[52:55], v[148:151], 0
	s_waitcnt lgkmcnt(6)
	v_mfma_f32_32x32x16_f16 v[84:99], v[56:59], v[120:123], v[84:99]
	v_mfma_f32_32x32x16_f16 v[100:115], v[56:59], v[152:155], v[100:115]
	s_waitcnt lgkmcnt(5)
	v_mfma_f32_32x32x16_f16 v[84:99], v[60:63], v[124:127], v[84:99]
	v_mfma_f32_32x32x16_f16 v[100:115], v[60:63], v[156:159], v[100:115]
	s_waitcnt lgkmcnt(4)
	v_mfma_f32_32x32x16_f16 v[84:99], v[64:67], v[128:131], v[84:99]
	v_mfma_f32_32x32x16_f16 v[100:115], v[64:67], v[160:163], v[100:115]
	s_waitcnt lgkmcnt(3)
	v_mfma_f32_32x32x16_f16 v[84:99], v[68:71], v[132:135], v[84:99]
	v_mfma_f32_32x32x16_f16 v[100:115], v[68:71], v[164:167], v[100:115]
	s_waitcnt lgkmcnt(2)
	v_mfma_f32_32x32x16_f16 v[84:99], v[72:75], v[136:139], v[84:99]
	v_mfma_f32_32x32x16_f16 v[100:115], v[72:75], v[168:171], v[100:115]
	s_waitcnt lgkmcnt(1)
	v_mfma_f32_32x32x16_f16 v[84:99], v[76:79], v[140:143], v[84:99]
	v_mfma_f32_32x32x16_f16 v[100:115], v[76:79], v[172:175], v[100:115]
	s_waitcnt lgkmcnt(0)
	v_mfma_f32_32x32x16_f16 v[84:99], v[80:83], v[144:147], v[84:99]
	v_mfma_f32_32x32x16_f16 v[100:115], v[80:83], v[176:179], v[100:115]
	s_nop 15
	v_add_f32_e32 v84, v84, v180
	v_max_f32_e32 v84, 0, v84
	buffer_store_dword v84, v17, s[28:31], 0 offen offset:0 nt sc1
	v_add_f32_e32 v85, v85, v180
	v_max_f32_e32 v85, 0, v85
	buffer_store_dword v85, v17, s[28:31], 0 offen offset:512 nt sc1
	v_add_f32_e32 v86, v86, v180
	v_max_f32_e32 v86, 0, v86
	buffer_store_dword v86, v17, s[28:31], 0 offen offset:1024 nt sc1
	v_add_f32_e32 v87, v87, v180
	v_max_f32_e32 v87, 0, v87
	buffer_store_dword v87, v17, s[28:31], 0 offen offset:1536 nt sc1
	v_add_f32_e32 v88, v88, v180
	v_max_f32_e32 v88, 0, v88
	buffer_store_dword v88, v17, s[28:31], s33 offen offset:0 nt sc1
	v_add_f32_e32 v89, v89, v180
	v_max_f32_e32 v89, 0, v89
	buffer_store_dword v89, v17, s[28:31], s33 offen offset:512 nt sc1
	v_add_f32_e32 v90, v90, v180
	v_max_f32_e32 v90, 0, v90
	buffer_store_dword v90, v17, s[28:31], s33 offen offset:1024 nt sc1
	v_add_f32_e32 v91, v91, v180
	v_max_f32_e32 v91, 0, v91
	buffer_store_dword v91, v17, s[28:31], s33 offen offset:1536 nt sc1
	v_add_f32_e32 v92, v92, v180
	v_max_f32_e32 v92, 0, v92
	buffer_store_dword v92, v17, s[28:31], s34 offen offset:0 nt sc1
	v_add_f32_e32 v93, v93, v180
	v_max_f32_e32 v93, 0, v93
	buffer_store_dword v93, v17, s[28:31], s34 offen offset:512 nt sc1
	v_add_f32_e32 v94, v94, v180
	v_max_f32_e32 v94, 0, v94
	buffer_store_dword v94, v17, s[28:31], s34 offen offset:1024 nt sc1
	v_add_f32_e32 v95, v95, v180
	v_max_f32_e32 v95, 0, v95
	buffer_store_dword v95, v17, s[28:31], s34 offen offset:1536 nt sc1
	v_add_f32_e32 v96, v96, v180
	v_max_f32_e32 v96, 0, v96
	buffer_store_dword v96, v17, s[28:31], s35 offen offset:0 nt sc1
	v_add_f32_e32 v97, v97, v180
	v_max_f32_e32 v97, 0, v97
	buffer_store_dword v97, v17, s[28:31], s35 offen offset:512 nt sc1
	v_add_f32_e32 v98, v98, v180
	v_max_f32_e32 v98, 0, v98
	buffer_store_dword v98, v17, s[28:31], s35 offen offset:1024 nt sc1
	v_add_f32_e32 v99, v99, v180
	v_max_f32_e32 v99, 0, v99
	buffer_store_dword v99, v17, s[28:31], s35 offen offset:1536 nt sc1
	v_add_f32_e32 v100, v100, v181
	v_max_f32_e32 v100, 0, v100
	buffer_store_dword v100, v17, s[28:31], 0 offen offset:128 nt sc1
	v_add_f32_e32 v101, v101, v181
	v_max_f32_e32 v101, 0, v101
	buffer_store_dword v101, v17, s[28:31], 0 offen offset:640 nt sc1
	v_add_f32_e32 v102, v102, v181
	v_max_f32_e32 v102, 0, v102
	buffer_store_dword v102, v17, s[28:31], 0 offen offset:1152 nt sc1
	v_add_f32_e32 v103, v103, v181
	v_max_f32_e32 v103, 0, v103
	buffer_store_dword v103, v17, s[28:31], 0 offen offset:1664 nt sc1
	v_add_f32_e32 v104, v104, v181
	v_max_f32_e32 v104, 0, v104
	buffer_store_dword v104, v17, s[28:31], s33 offen offset:128 nt sc1
	v_add_f32_e32 v105, v105, v181
	v_max_f32_e32 v105, 0, v105
	buffer_store_dword v105, v17, s[28:31], s33 offen offset:640 nt sc1
	v_add_f32_e32 v106, v106, v181
	v_max_f32_e32 v106, 0, v106
	buffer_store_dword v106, v17, s[28:31], s33 offen offset:1152 nt sc1
	v_add_f32_e32 v107, v107, v181
	v_max_f32_e32 v107, 0, v107
	buffer_store_dword v107, v17, s[28:31], s33 offen offset:1664 nt sc1
	v_add_f32_e32 v108, v108, v181
	v_max_f32_e32 v108, 0, v108
	buffer_store_dword v108, v17, s[28:31], s34 offen offset:128 nt sc1
	v_add_f32_e32 v109, v109, v181
	v_max_f32_e32 v109, 0, v109
	buffer_store_dword v109, v17, s[28:31], s34 offen offset:640 nt sc1
	v_add_f32_e32 v110, v110, v181
	v_max_f32_e32 v110, 0, v110
	buffer_store_dword v110, v17, s[28:31], s34 offen offset:1152 nt sc1
	v_add_f32_e32 v111, v111, v181
	v_max_f32_e32 v111, 0, v111
	buffer_store_dword v111, v17, s[28:31], s34 offen offset:1664 nt sc1
	v_add_f32_e32 v112, v112, v181
	v_max_f32_e32 v112, 0, v112
	buffer_store_dword v112, v17, s[28:31], s35 offen offset:128 nt sc1
	v_add_f32_e32 v113, v113, v181
	v_max_f32_e32 v113, 0, v113
	buffer_store_dword v113, v17, s[28:31], s35 offen offset:640 nt sc1
	v_add_f32_e32 v114, v114, v181
	v_max_f32_e32 v114, 0, v114
	buffer_store_dword v114, v17, s[28:31], s35 offen offset:1152 nt sc1
	v_add_f32_e32 v115, v115, v181
	v_max_f32_e32 v115, 0, v115
	buffer_store_dword v115, v17, s[28:31], s35 offen offset:1664 nt sc1
	s_endpgm

	.amdhsa_kernel _Z19combine_proj_kernelPKDF16_PK15HIP_vector_typeIfLj2EES0_PKfPf
		.amdhsa_group_segment_fixed_size 17408
		.amdhsa_private_segment_fixed_size 0
		.amdhsa_kernarg_size 40
		.amdhsa_user_sgpr_count 2
		.amdhsa_user_sgpr_dispatch_ptr 0
		.amdhsa_user_sgpr_queue_ptr 0
		.amdhsa_user_sgpr_kernarg_segment_ptr 1
		.amdhsa_user_sgpr_dispatch_id 0
		.amdhsa_user_sgpr_kernarg_preload_length 0
		.amdhsa_user_sgpr_kernarg_preload_offset 0
		.amdhsa_user_sgpr_private_segment_size 0
		.amdhsa_uses_dynamic_stack 0
		.amdhsa_enable_private_segment 0
		.amdhsa_system_sgpr_workgroup_id_x 1
		.amdhsa_system_sgpr_workgroup_id_y 0
		.amdhsa_system_sgpr_workgroup_id_z 0
		.amdhsa_system_sgpr_workgroup_info 0
		.amdhsa_system_vgpr_workitem_id 0
		.amdhsa_next_free_vgpr 208
		.amdhsa_next_free_sgpr 36
		.amdhsa_accum_offset 204
		.amdhsa_reserve_vcc 1
		.amdhsa_float_round_mode_32 0
		.amdhsa_float_round_mode_16_64 0
		.amdhsa_float_denorm_mode_32 3
		.amdhsa_float_denorm_mode_16_64 3
		.amdhsa_dx10_clamp 1
		.amdhsa_ieee_mode 1
		.amdhsa_fp16_overflow 0
		.amdhsa_tg_split 0
		.amdhsa_exception_fp_ieee_invalid_op 0
		.amdhsa_exception_fp_denorm_src 0
		.amdhsa_exception_fp_ieee_div_zero 0
		.amdhsa_exception_fp_ieee_overflow 0
		.amdhsa_exception_fp_ieee_underflow 0
		.amdhsa_exception_fp_ieee_inexact 0
		.amdhsa_exception_int_div_zero 0
	.end_amdhsa_kernel

amdhsa.kernels:
  - .agpr_count:     32
    .args:
      - .actual_access:  read_only
        .address_space:  global
        .offset:         0
        .size:           8
        .value_kind:     global_buffer
      - .actual_access:  read_only
        .address_space:  global
        .offset:         8
        .size:           8
        .value_kind:     global_buffer
      - .actual_access:  read_only
        .address_space:  global
        .offset:         16
        .size:           8
        .value_kind:     global_buffer
      - .actual_access:  read_only
        .address_space:  global
        .offset:         24
        .size:           8
        .value_kind:     global_buffer
      - .actual_access:  write_only
        .address_space:  global
        .offset:         32
        .size:           8
        .value_kind:     global_buffer
      - .actual_access:  write_only
        .address_space:  global
        .offset:         40
        .size:           8
        .value_kind:     global_buffer
      - .actual_access:  read_only
        .address_space:  global
        .offset:         48
        .size:           8
        .value_kind:     global_buffer
      - .actual_access:  write_only
        .address_space:  global
        .offset:         56
        .size:           8
        .value_kind:     global_buffer
    .group_segment_fixed_size: 34816
    .kernarg_segment_align: 8
    .kernarg_segment_size: 64
    .language:       OpenCL C
    .language_version:
      - 2
      - 0
    .max_flat_workgroup_size: 256
    .name:           _Z11prep_kernelPKfS0_S0_S0_PDF16_S1_S0_S1_
    .private_segment_fixed_size: 0
    .sgpr_count:     30
    .sgpr_spill_count: 0
    .symbol:         _Z11prep_kernelPKfS0_S0_S0_PDF16_S1_S0_S1_.kd
    .uniform_work_group_size: 1
    .uses_dynamic_stack: false
    .vgpr_count:     208
    .vgpr_spill_count: 0
    .wavefront_size: 64
  - .agpr_count:     0
    .args:
      - .actual_access:  read_only
        .address_space:  global
        .offset:         0
        .size:           8
        .value_kind:     global_buffer
      - .address_space:  global
        .offset:         8
        .size:           8
        .value_kind:     global_buffer
      - .actual_access:  write_only
        .address_space:  global
        .offset:         16
        .size:           8
        .value_kind:     global_buffer
      - .actual_access:  write_only
        .address_space:  global
        .offset:         24
        .size:           8
        .value_kind:     global_buffer
    .group_segment_fixed_size: 0
    .kernarg_segment_align: 8
    .kernarg_segment_size: 32
    .language:       OpenCL C
    .language_version:
      - 2
      - 0
    .max_flat_workgroup_size: 512
    .name:           _Z11attn_kernelPKDF16_S0_PDF16_P15HIP_vector_typeIfLj2EE
    .private_segment_fixed_size: 0
    .sgpr_count:     46
    .sgpr_spill_count: 0
    .symbol:         _Z11attn_kernelPKDF16_S0_PDF16_P15HIP_vector_typeIfLj2EE.kd
    .uniform_work_group_size: 1
    .uses_dynamic_stack: false
    .vgpr_count:     244
    .vgpr_spill_count: 0
    .wavefront_size: 64
  - .agpr_count:     0
    .args:
      - .actual_access:  read_only
        .address_space:  global
        .offset:         0
        .size:           8
        .value_kind:     global_buffer
      - .actual_access:  read_only
        .address_space:  global
        .offset:         8
        .size:           8
        .value_kind:     global_buffer
      - .actual_access:  read_only
        .address_space:  global
        .offset:         16
        .size:           8
        .value_kind:     global_buffer
      - .actual_access:  read_only
        .address_space:  global
        .offset:         24
        .size:           8
        .value_kind:     global_buffer
      - .actual_access:  write_only
        .address_space:  global
        .offset:         32
        .size:           8
        .value_kind:     global_buffer
    .group_segment_fixed_size: 17408
    .kernarg_segment_align: 8
    .kernarg_segment_size: 40
    .language:       OpenCL C
    .language_version:
      - 2
      - 0
    .max_flat_workgroup_size: 256
    .name:           _Z19combine_proj_kernelPKDF16_PK15HIP_vector_typeIfLj2EES0_PKfPf
    .private_segment_fixed_size: 0
    .sgpr_count:     42
    .sgpr_spill_count: 0
    .symbol:         _Z19combine_proj_kernelPKDF16_PK15HIP_vector_typeIfLj2EES0_PKfPf.kd
    .uniform_work_group_size: 1
    .uses_dynamic_stack: false
    .vgpr_count:     208
    .vgpr_spill_count: 0
    .wavefront_size: 64
